# speedup vs baseline: 1.0131x; 1.0037x over previous
.LBB1_3:
	v_mov_b32_e32 v156, v0
	s_nop 0
	v_ashrrev_i32_e32 v157, 31, v156
	v_and_b32_e32 v167, 63, v156
	v_lshl_add_u64 v[6:7], v[156:157], 3, s[10:11]
	v_lshlrev_b32_e32 v169, 3, v167
	s_cmp_lt_i32 s22, 0
	s_cbranch_scc0 .Lskip_tabld
	global_load_dwordx2 v[4:5], v[6:7], off
	global_load_dwordx2 v[2:3], v169, s[10:11] offset:2048
.Lskip_tabld:
	v_readfirstlane_b32 s4, v156
	s_ashr_i32 s27, s4, 7
	s_lshl_b32 s0, s27, 1
	s_ashr_i32 s1, s0, 31
	s_lshl_b64 s[2:3], s[0:1], 13
	s_add_u32 s2, s8, s2
	s_addc_u32 s3, s9, s3
	s_add_u32 s28, s2, 0x18000
	s_addc_u32 s29, s3, 0
	v_lshlrev_b32_e32 v154, 4, v167
	v_lshl_add_u64 v[6:7], s[28:29], 0, v[154:155]
	v_or_b32_e32 v8, 0x800, v169
	v_add_co_u32_e32 v6, vcc, s23, v6
	v_lshlrev_b32_e32 v168, 1, v8
	s_nop 0
	v_addc_co_u32_e32 v7, vcc, 0, v7, vcc
	global_load_dwordx4 v[150:153], v154, s[28:29]
	global_load_dwordx4 v[146:149], v154, s[28:29] offset:1024
	global_load_dwordx4 v[142:145], v154, s[28:29] offset:2048
	global_load_dwordx4 v[138:141], v154, s[28:29] offset:3072
	global_load_dwordx4 v[126:129], v[6:7], off offset:1024
	global_load_dwordx4 v[122:125], v[6:7], off offset:2048
	global_load_dwordx4 v[134:137], v168, s[28:29]
	global_load_dwordx4 v[130:133], v[6:7], off offset:3072
	v_lshl_add_u64 v[6:7], s[2:3], 0, v[154:155]
	v_lshl_add_u64 v[8:9], v[6:7], 0, s[16:17]
	v_add_co_u32_e32 v6, vcc, 0x28000, v6
	s_nop 1
	v_addc_co_u32_e32 v7, vcc, 0, v7, vcc
	global_load_dwordx4 v[86:89], v[6:7], off
	global_load_dwordx4 v[82:85], v[8:9], off offset:1024
	v_cmp_gt_i32_e32 vcc, 16, v156
	v_lshl_add_u32 v166, v156, 2, v165
	s_and_saveexec_b64 s[2:3], vcc
	ds_write_b32 v166, v155
	s_or_b64 exec, exec, s[2:3]
	s_cmp_lt_i32 s22, 0
	s_cbranch_scc0 .Lskip_stage0
	v_lshl_add_u32 v6, v156, 3, v1
	v_cmp_gt_i32_e32 vcc, 64, v156
	s_waitcnt vmcnt(11)
	ds_write_b64 v6, v[4:5]
	s_and_saveexec_b64 s[2:3], vcc
	s_cbranch_execz .LBB1_7
	s_waitcnt vmcnt(10)
	ds_write_b64 v6, v[2:3] offset:2048

.Lskip_stage0:
	s_waitcnt vmcnt(10)
	s_ashr_i32 s2, s4, 6
	s_lshl_b32 s3, s2, 3
	s_and_b32 s5, s3, 8
	s_bfe_u32 s26, s2, 0x10001
	s_or_b32 s5, s26, s5
	s_lshl_b32 s26, s2, 9
	s_and_b32 s26, s26, 0x400
	s_lshl_b32 s5, s5, 4
	s_or_b32 s28, s5, s26
	v_lshrrev_b32_e32 v182, 5, v167
	v_bfe_u32 v2, v156, 4, 1
	v_bitop3_b32 v3, v182, v156, 1 bitop3:0x78
	v_lshlrev_b32_e32 v154, 2, v182
	v_xor_b32_e32 v3, v3, v2
	v_bitop3_b32 v4, v154, v156, 4 bitop3:0x78
	v_and_b32_e32 v5, 10, v156
	v_or3_b32 v3, v5, v4, v3
	s_lshl_b32 s5, s2, 4
	v_lshlrev_b32_e32 v3, 4, v3
	s_lshl_b32 s3, s2, 13
	s_and_b32 s29, s5, 16
	v_lshlrev_b32_e32 v170, 8, v182
	v_lshl_or_b32 v171, v2, 10, v3
	s_or_b32 s26, s29, s3
	v_bitop3_b32 v179, v171, s26, v170 bitop3:0x36
	s_or_b32 s5, s26, 0x280
	v_bitop3_b32 v178, v171, s5, v170 bitop3:0x36
	s_or_b32 s30, s3, 0x800
	s_or_b32 s33, s3, 0x1000
	s_or_b32 s29, s29, 64
	s_or_b32 s34, s29, s33
	v_bitop3_b32 v180, v171, s34, v170 bitop3:0x36
	s_or_b32 s29, s3, s29
	s_or_b32 s29, s29, 0x1280
	s_and_b32 s5, s2, 1
	s_lshl_b32 s31, s5, 4
	s_or_b32 s2, s31, s3
	v_bitop3_b32 v173, v171, s2, v170 bitop3:0x36
	v_bitop3_b32 v34, v156, 31, v156 bitop3:0xc
	v_lshrrev_b32_e32 v35, 4, v34
	v_bitop3_b32 v36, v34, v182, 1 bitop3:0x6c
	v_xor_b32_e32 v36, v36, v35
	v_bitop3_b32 v34, v34, v154, 4 bitop3:0x6c
	v_bitop3_b32 v37, v156, 10, 31 bitop3:8
	v_or3_b32 v34, v37, v34, v36
	v_lshlrev_b32_e32 v35, 10, v35
	v_lshlrev_b32_e32 v34, 4, v34
	v_or3_b32 v154, v35, v34, v170
	v_bitop3_b32 v172, s2, v154, v159 bitop3:0x36
	v_bitop3_b32 v176, v171, s29, v170 bitop3:0x36
	s_or_b32 s29, s31, s30
	s_or_b32 s29, s29, 0xa0
	v_bitop3_b32 v175, v171, s29, v170 bitop3:0x36
	s_or_b32 s29, s2, 0xaa0
	s_xor_b32 s29, s29, 0x80
	v_xor_b32_e32 v174, s29, v154
	s_or_b32 s29, s26, 0x18e0
	v_bitop3_b32 v181, v171, s29, v170 bitop3:0x36
	s_or_b32 s29, s26, 0x1a60
	v_bitop3_b32 v177, v171, s29, v170 bitop3:0x36
	s_or_b32 s29, s31, 64
	s_or_b32 s3, s3, s29
	s_mov_b32 s41, s3
	s_or_b32 s29, s29, s33
	s_mov_b32 s40, s29
	s_or_b32 s3, s2, 0x18e0
	s_mov_b32 s42, s3
	s_or_b32 s2, s2, 0x1ae0
	s_xor_b32 s2, s2, 0x80
	s_mov_b32 s43, s2
	s_lshr_b32 s38, s4, 1
	v_and_b32_e32 v26, 31, v167
	v_and_b32_e32 v27, 3, v167
	v_bfe_u32 v28, v167, 3, 1
	v_bfe_u32 v29, v167, 2, 1
	v_lshl_or_b32 v27, v28, 2, v27
	v_lshl_or_b32 v27, v29, 3, v27
	v_lshlrev_b32_e32 v32, 9, v182
	v_lshl_add_u32 v30, v27, 3, v32
	v_add_u32_e32 v30, 0x10000, v30
	v_lshl_add_u32 v31, v26, 3, v32
	v_add_u32_e32 v31, 0x10400, v31
	v_xor_b32_e32 v28, 31, v26
	v_lshl_add_u32 v28, v28, 3, v32
	v_add_u32_e32 v28, 0x10400, v28
	v_bfe_u32 v29, v167, 4, 1
	v_mul_u32_u24_e32 v29, 0x78, v29
	v_xor_b32_e32 v254, s38, v29
	v_or_b32_e32 v254, 0x10800, v254
	v_and_b32_e32 v33, 16, v167
	v_cmp_eq_u32_e32 vcc, 0, v33
	ds_read2_b64 v[66:69], v30 offset0:0 offset1:32
	ds_read2_b64 v[70:73], v30 offset0:16 offset1:48
	ds_read2_b64 v[198:201], v31 offset0:0 offset1:32
	ds_read2_b64 v[202:205], v28 offset0:0 offset1:32
	ds_read2_b64 v[206:209], v254 offset0:0 offset1:16
	ds_read2_b64 v[210:213], v254 offset0:32 offset1:48
	s_waitcnt lgkmcnt(0)
	v_cndmask_b32_e32 v74, v67, v66, vcc
	v_cndmask_b32_e32 v75, v69, v68, vcc
	v_cndmask_b32_e64 v76, v66, -v67, vcc
	v_cndmask_b32_e64 v77, v68, -v69, vcc
	v_cndmask_b32_e32 v78, v71, v70, vcc
	v_cndmask_b32_e32 v79, v73, v72, vcc
	v_cndmask_b32_e64 v80, v70, -v71, vcc
	v_cndmask_b32_e64 v81, v72, -v73, vcc
	v_cvt_pk_f16_f32 v190, v74, v75
	v_cvt_pk_f16_f32 v191, v74, v75
	v_cvt_pk_f16_f32 v192, v76, v77
	v_cvt_pk_f16_f32 v193, v76, v77
	v_cvt_pk_f16_f32 v194, v78, v79
	v_cvt_pk_f16_f32 v195, v78, v79
	v_cvt_pk_f16_f32 v196, v80, v81
	v_cvt_pk_f16_f32 v197, v80, v81
	v_mul_f32_e32 v66, v199, v207
	v_mul_f32_e32 v68, v199, v206
	v_mul_f32_e32 v67, v199, v209
	v_mul_f32_e32 v69, v199, v208
	v_fma_f32 v66, v198, v206, -v66
	v_fma_f32 v68, v198, v207, v68
	v_fma_f32 v67, v198, v208, -v67
	v_fma_f32 v69, v198, v209, v69
	v_cvt_pk_f16_f32 v214, v66, v67
	v_cvt_pk_f16_f32 v216, v68, v69
	v_mul_f32_e32 v70, v201, v211
	v_mul_f32_e32 v72, v201, v210
	v_mul_f32_e32 v71, v201, v213
	v_mul_f32_e32 v73, v201, v212
	v_fma_f32 v70, v200, v210, -v70
	v_fma_f32 v72, v200, v211, v72
	v_fma_f32 v71, v200, v212, -v71
	v_fma_f32 v73, v200, v213, v73
	v_cvt_pk_f16_f32 v215, v70, v71
	v_cvt_pk_f16_f32 v217, v72, v73
	v_mul_f32_e32 v66, v203, v207
	v_mul_f32_e32 v68, v203, v206
	v_mul_f32_e32 v67, v203, v209
	v_mul_f32_e32 v69, v203, v208
	v_fma_f32 v66, v202, v206, -v66
	v_fma_f32 v68, v202, v207, v68
	v_fma_f32 v67, v202, v208, -v67
	v_fma_f32 v69, v202, v209, v69
	v_cvt_pk_f16_f32 v218, v66, v67
	v_cvt_pk_f16_f32 v220, v68, v69
	v_mul_f32_e32 v70, v205, v211
	v_mul_f32_e32 v72, v205, v210
	v_mul_f32_e32 v71, v205, v213
	v_mul_f32_e32 v73, v205, v212
	v_fma_f32 v70, v204, v210, -v70
	v_fma_f32 v72, v204, v211, v72
	v_fma_f32 v71, v204, v212, -v71
	v_fma_f32 v73, v204, v213, v73
	v_cvt_pk_f16_f32 v219, v70, v71
	v_cvt_pk_f16_f32 v221, v72, v73
	v_xor_b32_e32 v255, 8, v254
	ds_read2_b64 v[206:209], v255 offset0:0 offset1:16
	ds_read2_b64 v[210:213], v255 offset0:32 offset1:48
	v_mfma_f32_32x32x16_f16 v[2:17], v[190:193], v[214:217], 0
	v_mfma_f32_32x32x16_f16 v[18:33], v[194:197], v[218:221], 0
	s_waitcnt lgkmcnt(0)
	v_mul_f32_e32 v66, v199, v207
	v_mul_f32_e32 v68, v199, v206
	v_mul_f32_e32 v67, v199, v209
	v_mul_f32_e32 v69, v199, v208
	v_fma_f32 v66, v198, v206, -v66
	v_fma_f32 v68, v198, v207, v68
	v_fma_f32 v67, v198, v208, -v67
	v_fma_f32 v69, v198, v209, v69
	v_cvt_pk_f16_f32 v214, v66, v67
	v_cvt_pk_f16_f32 v216, v68, v69
	v_mul_f32_e32 v70, v201, v211
	v_mul_f32_e32 v72, v201, v210
	v_mul_f32_e32 v71, v201, v213
	v_mul_f32_e32 v73, v201, v212
	v_fma_f32 v70, v200, v210, -v70
	v_fma_f32 v72, v200, v211, v72
	v_fma_f32 v71, v200, v212, -v71
	v_fma_f32 v73, v200, v213, v73
	v_cvt_pk_f16_f32 v215, v70, v71
	v_cvt_pk_f16_f32 v217, v72, v73
	v_cvt_pk_f16_f32 v2, v2, v3
	v_cvt_pk_f16_f32 v3, v4, v5
	v_cvt_pk_f16_f32 v4, v6, v7
	v_cvt_pk_f16_f32 v5, v8, v9
	v_cvt_pk_f16_f32 v6, v10, v11
	v_cvt_pk_f16_f32 v7, v12, v13
	v_cvt_pk_f16_f32 v8, v14, v15
	v_cvt_pk_f16_f32 v9, v16, v17
	v_cvt_pk_f16_f32 v18, v18, v19
	v_cvt_pk_f16_f32 v19, v20, v21
	v_cvt_pk_f16_f32 v20, v22, v23
	v_cvt_pk_f16_f32 v21, v24, v25
	v_cvt_pk_f16_f32 v22, v26, v27
	v_cvt_pk_f16_f32 v23, v28, v29
	v_cvt_pk_f16_f32 v24, v30, v31
	v_cvt_pk_f16_f32 v25, v32, v33
	s_setprio 1
	s_waitcnt vmcnt(6)
	v_mul_f32_e32 v66, v203, v207
	v_mul_f32_e32 v68, v203, v206
	v_mfma_f32_32x32x16_f16 v[34:49], v[2:5], v[150:153], 0
	v_mul_f32_e32 v67, v203, v209
	v_mul_f32_e32 v69, v203, v208
	v_mfma_f32_32x32x16_f16 v[34:49], v[18:21], v[146:149], v[34:49]
	v_fma_f32 v66, v202, v206, -v66
	v_fma_f32 v68, v202, v207, v68
	v_mfma_f32_32x32x16_f16 v[34:49], v[6:9], v[142:145], v[34:49]
	v_fma_f32 v67, v202, v208, -v67
	v_fma_f32 v69, v202, v209, v69
	v_mfma_f32_32x32x16_f16 v[34:49], v[22:25], v[138:141], v[34:49]
	v_cvt_pk_f16_f32 v218, v66, v67
	v_cvt_pk_f16_f32 v220, v68, v69
	s_waitcnt vmcnt(2)
	v_mul_f32_e32 v70, v205, v211
	v_mul_f32_e32 v72, v205, v210
	v_mfma_f32_32x32x16_f16 v[50:65], v[2:5], v[134:137], 0
	v_mul_f32_e32 v71, v205, v213
	v_mul_f32_e32 v73, v205, v212
	v_mfma_f32_32x32x16_f16 v[50:65], v[18:21], v[126:129], v[50:65]
	v_fma_f32 v70, v204, v210, -v70
	v_fma_f32 v72, v204, v211, v72
	v_mfma_f32_32x32x16_f16 v[50:65], v[6:9], v[122:125], v[50:65]
	v_fma_f32 v71, v204, v212, -v71
	v_fma_f32 v73, v204, v213, v73
	v_mfma_f32_32x32x16_f16 v[50:65], v[22:25], v[130:133], v[50:65]
	v_cvt_pk_f16_f32 v219, v70, v71
	v_cvt_pk_f16_f32 v221, v72, v73
	v_xor_b32_e32 v255, 16, v254
	ds_read2_b64 v[206:209], v255 offset0:0 offset1:16
	ds_read2_b64 v[210:213], v255 offset0:32 offset1:48
	v_mfma_f32_32x32x16_f16 v[2:17], v[190:193], v[214:217], 0
	v_mfma_f32_32x32x16_f16 v[18:33], v[194:197], v[218:221], 0
	v_cvt_pk_f16_f32 v34, v34, v35
	v_cvt_pk_f16_f32 v35, v36, v37
	v_cvt_pk_f16_f32 v36, v38, v39
	v_cvt_pk_f16_f32 v37, v40, v41
	v_cvt_pk_f16_f32 v38, v42, v43
	v_cvt_pk_f16_f32 v39, v44, v45
	v_cvt_pk_f16_f32 v40, v46, v47
	v_cvt_pk_f16_f32 v41, v48, v49
	v_cvt_pk_f16_f32 v50, v50, v51
	v_cvt_pk_f16_f32 v51, v52, v53
	v_cvt_pk_f16_f32 v52, v54, v55
	v_cvt_pk_f16_f32 v53, v56, v57
	v_cvt_pk_f16_f32 v54, v58, v59
	v_cvt_pk_f16_f32 v55, v60, v61
	v_cvt_pk_f16_f32 v56, v62, v63
	v_cvt_pk_f16_f32 v57, v64, v65
	s_waitcnt vmcnt(2)
	v_cvt_pk_f16_f32 v2, v2, v3
	v_cvt_pk_f16_f32 v3, v4, v5
	v_cvt_pk_f16_f32 v4, v6, v7
	v_cvt_pk_f16_f32 v5, v8, v9
	v_mfma_f32_32x32x16_f16 v[90:105], v[34:37], v[222:225], 0
	v_cvt_pk_f16_f32 v6, v10, v11
	v_cvt_pk_f16_f32 v7, v12, v13
	v_cvt_pk_f16_f32 v8, v14, v15
	v_cvt_pk_f16_f32 v9, v16, v17
	v_mfma_f32_32x32x16_f16 v[106:121], v[34:37], v[238:241], 0
	v_cvt_pk_f16_f32 v18, v18, v19
	v_cvt_pk_f16_f32 v19, v20, v21
	v_cvt_pk_f16_f32 v20, v22, v23
	v_cvt_pk_f16_f32 v21, v24, v25
	v_mfma_f32_32x32x16_f16 v[90:105], v[38:41], v[226:229], v[90:105]
	v_cvt_pk_f16_f32 v22, v26, v27
	v_cvt_pk_f16_f32 v23, v28, v29
	v_cvt_pk_f16_f32 v24, v30, v31
	v_cvt_pk_f16_f32 v25, v32, v33
	v_mfma_f32_32x32x16_f16 v[106:121], v[38:41], v[242:245], v[106:121]
	s_waitcnt lgkmcnt(0)
	v_mul_f32_e32 v66, v199, v207
	v_mul_f32_e32 v68, v199, v206
	v_mul_f32_e32 v67, v199, v209
	v_mfma_f32_32x32x16_f16 v[90:105], v[50:53], v[230:233], v[90:105]
	v_mul_f32_e32 v69, v199, v208
	v_fma_f32 v66, v198, v206, -v66
	v_fma_f32 v68, v198, v207, v68
	v_fma_f32 v67, v198, v208, -v67
	v_mfma_f32_32x32x16_f16 v[106:121], v[50:53], v[246:249], v[106:121]
	v_fma_f32 v69, v198, v209, v69
	v_cvt_pk_f16_f32 v214, v66, v67
	v_cvt_pk_f16_f32 v216, v68, v69
	v_mul_f32_e32 v70, v201, v211
	v_mfma_f32_32x32x16_f16 v[90:105], v[54:57], v[234:237], v[90:105]
	v_mul_f32_e32 v72, v201, v210
	v_mul_f32_e32 v71, v201, v213
	v_mul_f32_e32 v73, v201, v212
	v_fma_f32 v70, v200, v210, -v70
	v_mfma_f32_32x32x16_f16 v[106:121], v[54:57], v[250:253], v[106:121]
	v_fma_f32 v72, v200, v211, v72
	v_fma_f32 v71, v200, v212, -v71
	v_fma_f32 v73, v200, v213, v73
	v_cvt_pk_f16_f32 v215, v70, v71
	v_cvt_pk_f16_f32 v217, v72, v73
	v_mfma_f32_32x32x16_f16 v[34:49], v[2:5], v[150:153], 0
	v_mul_f32_e32 v66, v203, v207
	v_mul_f32_e32 v68, v203, v206
	v_mul_f32_e32 v67, v203, v209
	v_mul_f32_e32 v69, v203, v208
	v_fma_f32 v66, v202, v206, -v66
	v_mfma_f32_32x32x16_f16 v[34:49], v[18:21], v[146:149], v[34:49]
	v_fma_f32 v68, v202, v207, v68
	v_fma_f32 v67, v202, v208, -v67
	v_fma_f32 v69, v202, v209, v69
	v_cvt_pk_f16_f32 v218, v66, v67
	v_cvt_pk_f16_f32 v220, v68, v69
	v_mfma_f32_32x32x16_f16 v[34:49], v[6:9], v[142:145], v[34:49]
	v_mul_f32_e32 v70, v205, v211
	v_mul_f32_e32 v72, v205, v210
	v_mul_f32_e32 v71, v205, v213
	v_mul_f32_e32 v73, v205, v212
	v_fma_f32 v70, v204, v210, -v70
	v_mfma_f32_32x32x16_f16 v[34:49], v[22:25], v[138:141], v[34:49]
	v_fma_f32 v72, v204, v211, v72
	v_fma_f32 v71, v204, v212, -v71
	v_fma_f32 v73, v204, v213, v73
	v_cvt_pk_f16_f32 v219, v70, v71
	v_cvt_pk_f16_f32 v221, v72, v73
	v_mfma_f32_32x32x16_f16 v[50:65], v[2:5], v[134:137], 0
	v_cvt_pk_f16_f32 v90, v90, v91
	v_cvt_pk_f16_f32 v91, v92, v93
	v_cvt_pk_f16_f32 v92, v94, v95
	v_cvt_pk_f16_f32 v93, v96, v97
	v_cvt_pk_f16_f32 v94, v98, v99
	v_mfma_f32_32x32x16_f16 v[50:65], v[18:21], v[126:129], v[50:65]
	v_cvt_pk_f16_f32 v95, v100, v101
	v_cvt_pk_f16_f32 v96, v102, v103
	v_cvt_pk_f16_f32 v97, v104, v105
	v_cvt_pk_f16_f32 v106, v106, v107
	v_cvt_pk_f16_f32 v107, v108, v109
	v_mfma_f32_32x32x16_f16 v[50:65], v[6:9], v[122:125], v[50:65]
	v_cvt_pk_f16_f32 v108, v110, v111
	v_cvt_pk_f16_f32 v109, v112, v113
	v_cvt_pk_f16_f32 v110, v114, v115
	v_cvt_pk_f16_f32 v111, v116, v117
	v_cvt_pk_f16_f32 v112, v118, v119
	v_mfma_f32_32x32x16_f16 v[50:65], v[22:25], v[130:133], v[50:65]
	v_cvt_pk_f16_f32 v113, v120, v121
	ds_write_b128 v173, v[90:93]
	ds_write_b128 v172, v[94:97]
	ds_write_b128 v173, v[106:109] offset:32768
	ds_write_b128 v172, v[110:113] offset:32768
	v_xor_b32_e32 v255, 24, v254
	ds_read2_b64 v[206:209], v255 offset0:0 offset1:16
	ds_read2_b64 v[210:213], v255 offset0:32 offset1:48
	v_mfma_f32_32x32x16_f16 v[2:17], v[190:193], v[214:217], 0
	v_mfma_f32_32x32x16_f16 v[18:33], v[194:197], v[218:221], 0
	v_cvt_pk_f16_f32 v34, v34, v35
	v_cvt_pk_f16_f32 v35, v36, v37
	v_cvt_pk_f16_f32 v36, v38, v39
	v_cvt_pk_f16_f32 v37, v40, v41
	v_cvt_pk_f16_f32 v38, v42, v43
	v_cvt_pk_f16_f32 v39, v44, v45
	v_cvt_pk_f16_f32 v40, v46, v47
	v_cvt_pk_f16_f32 v41, v48, v49
	v_cvt_pk_f16_f32 v50, v50, v51
	v_cvt_pk_f16_f32 v51, v52, v53
	v_cvt_pk_f16_f32 v52, v54, v55
	v_cvt_pk_f16_f32 v53, v56, v57
	v_cvt_pk_f16_f32 v54, v58, v59
	v_cvt_pk_f16_f32 v55, v60, v61
	v_cvt_pk_f16_f32 v56, v62, v63
	v_cvt_pk_f16_f32 v57, v64, v65
	v_mfma_f32_32x32x16_f16 v[90:105], v[34:37], v[222:225], 0
	v_cvt_pk_f16_f32 v2, v2, v3
	v_cvt_pk_f16_f32 v3, v4, v5
	v_cvt_pk_f16_f32 v4, v6, v7
	v_cvt_pk_f16_f32 v5, v8, v9
	v_mfma_f32_32x32x16_f16 v[106:121], v[34:37], v[238:241], 0
	v_cvt_pk_f16_f32 v6, v10, v11
	v_cvt_pk_f16_f32 v7, v12, v13
	v_cvt_pk_f16_f32 v8, v14, v15
	v_cvt_pk_f16_f32 v9, v16, v17
	v_cvt_pk_f16_f32 v18, v18, v19
	v_mfma_f32_32x32x16_f16 v[90:105], v[38:41], v[226:229], v[90:105]
	v_cvt_pk_f16_f32 v19, v20, v21
	v_cvt_pk_f16_f32 v20, v22, v23
	v_cvt_pk_f16_f32 v21, v24, v25
	v_cvt_pk_f16_f32 v22, v26, v27
	v_mfma_f32_32x32x16_f16 v[106:121], v[38:41], v[242:245], v[106:121]
	v_cvt_pk_f16_f32 v23, v28, v29
	v_cvt_pk_f16_f32 v24, v30, v31
	v_cvt_pk_f16_f32 v25, v32, v33
	s_waitcnt lgkmcnt(0)
	v_mul_f32_e32 v66, v199, v207
	v_mfma_f32_32x32x16_f16 v[90:105], v[50:53], v[230:233], v[90:105]
	v_mul_f32_e32 v68, v199, v206
	v_mul_f32_e32 v67, v199, v209
	v_mul_f32_e32 v69, v199, v208
	v_fma_f32 v66, v198, v206, -v66
	v_fma_f32 v68, v198, v207, v68
	v_mfma_f32_32x32x16_f16 v[106:121], v[50:53], v[246:249], v[106:121]
	v_fma_f32 v67, v198, v208, -v67
	v_fma_f32 v69, v198, v209, v69
	v_cvt_pk_f16_f32 v214, v66, v67
	v_cvt_pk_f16_f32 v216, v68, v69
	v_mfma_f32_32x32x16_f16 v[90:105], v[54:57], v[234:237], v[90:105]
	v_mul_f32_e32 v70, v201, v211
	v_mul_f32_e32 v72, v201, v210
	v_mul_f32_e32 v71, v201, v213
	v_mul_f32_e32 v73, v201, v212
	v_fma_f32 v70, v200, v210, -v70
	v_mfma_f32_32x32x16_f16 v[106:121], v[54:57], v[250:253], v[106:121]
	v_fma_f32 v72, v200, v211, v72
	v_fma_f32 v71, v200, v212, -v71
	v_fma_f32 v73, v200, v213, v73
	v_cvt_pk_f16_f32 v215, v70, v71
	v_cvt_pk_f16_f32 v217, v72, v73
	v_mfma_f32_32x32x16_f16 v[34:49], v[2:5], v[150:153], 0
	v_mul_f32_e32 v66, v203, v207
	v_mul_f32_e32 v68, v203, v206
	v_mul_f32_e32 v67, v203, v209
	v_mul_f32_e32 v69, v203, v208
	v_fma_f32 v66, v202, v206, -v66
	v_mfma_f32_32x32x16_f16 v[34:49], v[18:21], v[146:149], v[34:49]
	v_fma_f32 v68, v202, v207, v68
	v_fma_f32 v67, v202, v208, -v67
	v_fma_f32 v69, v202, v209, v69
	v_cvt_pk_f16_f32 v218, v66, v67
	v_cvt_pk_f16_f32 v220, v68, v69
	v_mfma_f32_32x32x16_f16 v[34:49], v[6:9], v[142:145], v[34:49]
	v_mul_f32_e32 v70, v205, v211
	v_mul_f32_e32 v72, v205, v210
	v_mul_f32_e32 v71, v205, v213
	v_mul_f32_e32 v73, v205, v212
	v_fma_f32 v70, v204, v210, -v70
	v_mfma_f32_32x32x16_f16 v[34:49], v[22:25], v[138:141], v[34:49]
	v_fma_f32 v72, v204, v211, v72
	v_fma_f32 v71, v204, v212, -v71
	v_fma_f32 v73, v204, v213, v73
	v_cvt_pk_f16_f32 v219, v70, v71
	v_cvt_pk_f16_f32 v221, v72, v73
	v_cvt_pk_f16_f32 v90, v90, v91
	v_mfma_f32_32x32x16_f16 v[50:65], v[2:5], v[134:137], 0
	v_cvt_pk_f16_f32 v91, v92, v93
	v_cvt_pk_f16_f32 v92, v94, v95
	v_cvt_pk_f16_f32 v93, v96, v97
	v_cvt_pk_f16_f32 v94, v98, v99
	v_cvt_pk_f16_f32 v95, v100, v101
	v_mfma_f32_32x32x16_f16 v[50:65], v[18:21], v[126:129], v[50:65]
	v_cvt_pk_f16_f32 v96, v102, v103
	v_cvt_pk_f16_f32 v97, v104, v105
	v_cvt_pk_f16_f32 v106, v106, v107
	v_cvt_pk_f16_f32 v107, v108, v109
	v_cvt_pk_f16_f32 v108, v110, v111
	v_mfma_f32_32x32x16_f16 v[50:65], v[6:9], v[122:125], v[50:65]
	v_cvt_pk_f16_f32 v109, v112, v113
	v_cvt_pk_f16_f32 v110, v114, v115
	v_cvt_pk_f16_f32 v111, v116, v117
	v_cvt_pk_f16_f32 v112, v118, v119
	v_cvt_pk_f16_f32 v113, v120, v121
	v_mfma_f32_32x32x16_f16 v[50:65], v[22:25], v[130:133], v[50:65]
	v_xor_b32_e32 v74, 0x8a0, v173
	v_xor_b32_e32 v75, 0x8a0, v172
	ds_write_b128 v74, v[90:93]
	ds_write_b128 v75, v[94:97]
	ds_write_b128 v74, v[106:109] offset:32768
	ds_write_b128 v75, v[110:113] offset:32768
	s_nop 0
	v_mfma_f32_32x32x16_f16 v[2:17], v[190:193], v[214:217], 0
	v_mfma_f32_32x32x16_f16 v[18:33], v[194:197], v[218:221], 0
	v_cvt_pk_f16_f32 v34, v34, v35
	v_cvt_pk_f16_f32 v35, v36, v37
	v_cvt_pk_f16_f32 v36, v38, v39
	v_cvt_pk_f16_f32 v37, v40, v41
	v_cvt_pk_f16_f32 v38, v42, v43
	v_cvt_pk_f16_f32 v39, v44, v45
	v_cvt_pk_f16_f32 v40, v46, v47
	v_cvt_pk_f16_f32 v41, v48, v49
	v_cvt_pk_f16_f32 v50, v50, v51
	v_cvt_pk_f16_f32 v51, v52, v53
	v_cvt_pk_f16_f32 v52, v54, v55
	v_cvt_pk_f16_f32 v53, v56, v57
	v_cvt_pk_f16_f32 v54, v58, v59
	v_cvt_pk_f16_f32 v55, v60, v61
	v_cvt_pk_f16_f32 v56, v62, v63
	v_cvt_pk_f16_f32 v57, v64, v65
	v_mfma_f32_32x32x16_f16 v[90:105], v[34:37], v[222:225], 0
	v_cvt_pk_f16_f32 v2, v2, v3
	v_cvt_pk_f16_f32 v3, v4, v5
	v_mfma_f32_32x32x16_f16 v[106:121], v[34:37], v[238:241], 0
	v_cvt_pk_f16_f32 v4, v6, v7
	v_cvt_pk_f16_f32 v5, v8, v9
	v_mfma_f32_32x32x16_f16 v[90:105], v[38:41], v[226:229], v[90:105]
	v_cvt_pk_f16_f32 v6, v10, v11
	v_cvt_pk_f16_f32 v7, v12, v13
	v_mfma_f32_32x32x16_f16 v[106:121], v[38:41], v[242:245], v[106:121]
	v_cvt_pk_f16_f32 v8, v14, v15
	v_cvt_pk_f16_f32 v9, v16, v17
	v_mfma_f32_32x32x16_f16 v[90:105], v[50:53], v[230:233], v[90:105]
	v_cvt_pk_f16_f32 v18, v18, v19
	v_cvt_pk_f16_f32 v19, v20, v21
	v_mfma_f32_32x32x16_f16 v[106:121], v[50:53], v[246:249], v[106:121]
	v_cvt_pk_f16_f32 v20, v22, v23
	v_cvt_pk_f16_f32 v21, v24, v25
	v_mfma_f32_32x32x16_f16 v[90:105], v[54:57], v[234:237], v[90:105]
	v_cvt_pk_f16_f32 v22, v26, v27
	v_cvt_pk_f16_f32 v23, v28, v29
	v_mfma_f32_32x32x16_f16 v[106:121], v[54:57], v[250:253], v[106:121]
	v_cvt_pk_f16_f32 v24, v30, v31
	v_cvt_pk_f16_f32 v25, v32, v33
	v_mfma_f32_32x32x16_f16 v[34:49], v[2:5], v[150:153], 0
	v_mfma_f32_32x32x16_f16 v[34:49], v[18:21], v[146:149], v[34:49]
	v_mfma_f32_32x32x16_f16 v[34:49], v[6:9], v[142:145], v[34:49]
	v_mfma_f32_32x32x16_f16 v[34:49], v[22:25], v[138:141], v[34:49]
	v_mfma_f32_32x32x16_f16 v[50:65], v[2:5], v[134:137], 0
	s_nop 5
	v_cvt_pk_f16_f32 v90, v90, v91
	v_cvt_pk_f16_f32 v91, v92, v93
	v_cvt_pk_f16_f32 v92, v94, v95
	v_cvt_pk_f16_f32 v93, v96, v97
	v_mfma_f32_32x32x16_f16 v[50:65], v[18:21], v[126:129], v[50:65]
	v_cvt_pk_f16_f32 v94, v98, v99
	v_cvt_pk_f16_f32 v95, v100, v101
	v_cvt_pk_f16_f32 v96, v102, v103
	v_cvt_pk_f16_f32 v97, v104, v105
	v_cvt_pk_f16_f32 v106, v106, v107
	v_cvt_pk_f16_f32 v107, v108, v109
	v_mfma_f32_32x32x16_f16 v[50:65], v[6:9], v[122:125], v[50:65]
	v_cvt_pk_f16_f32 v108, v110, v111
	v_cvt_pk_f16_f32 v109, v112, v113
	v_cvt_pk_f16_f32 v110, v114, v115
	v_cvt_pk_f16_f32 v111, v116, v117
	v_cvt_pk_f16_f32 v112, v118, v119
	v_cvt_pk_f16_f32 v113, v120, v121
	v_mfma_f32_32x32x16_f16 v[50:65], v[22:25], v[130:133], v[50:65]
	v_xor_b32_e32 v74, 0x1040, v173
	v_xor_b32_e32 v75, 0x1040, v172
	ds_write_b128 v74, v[90:93]
	ds_write_b128 v75, v[94:97]
	ds_write_b128 v74, v[106:109] offset:32768
	ds_write_b128 v75, v[110:113] offset:32768
	s_nop 11
	v_cvt_pk_f16_f32 v34, v34, v35
	v_cvt_pk_f16_f32 v35, v36, v37
	v_cvt_pk_f16_f32 v36, v38, v39
	v_cvt_pk_f16_f32 v37, v40, v41
	v_cvt_pk_f16_f32 v38, v42, v43
	v_cvt_pk_f16_f32 v39, v44, v45
	v_cvt_pk_f16_f32 v40, v46, v47
	v_cvt_pk_f16_f32 v41, v48, v49
	v_cvt_pk_f16_f32 v50, v50, v51
	v_cvt_pk_f16_f32 v51, v52, v53
	v_cvt_pk_f16_f32 v52, v54, v55
	v_cvt_pk_f16_f32 v53, v56, v57
	v_cvt_pk_f16_f32 v54, v58, v59
	v_cvt_pk_f16_f32 v55, v60, v61
	v_cvt_pk_f16_f32 v56, v62, v63
	v_cvt_pk_f16_f32 v57, v64, v65
	v_mfma_f32_32x32x16_f16 v[90:105], v[34:37], v[222:225], 0
	v_mfma_f32_32x32x16_f16 v[106:121], v[34:37], v[238:241], 0
	v_mfma_f32_32x32x16_f16 v[90:105], v[38:41], v[226:229], v[90:105]
	v_mfma_f32_32x32x16_f16 v[106:121], v[38:41], v[242:245], v[106:121]
	v_mfma_f32_32x32x16_f16 v[90:105], v[50:53], v[230:233], v[90:105]
	v_mfma_f32_32x32x16_f16 v[106:121], v[50:53], v[246:249], v[106:121]
	v_mfma_f32_32x32x16_f16 v[90:105], v[54:57], v[234:237], v[90:105]
	v_mfma_f32_32x32x16_f16 v[106:121], v[54:57], v[250:253], v[106:121]
	v_and_b32_e32 v134, 1, v156
	v_bitop3_b32 v132, v171, s40, v170 bitop3:0x36
	v_bitop3_b32 v131, s41, v154, v160 bitop3:0x36
	v_bitop3_b32 v135, v171, s42, v170 bitop3:0x36
	v_xor_b32_e32 v133, s43, v154
	v_and_b32_e32 v130, 4, v156
	s_lshl_b32 s2, s27, 3
	s_lshl_b32 s3, s5, 2
	s_or_b32 s2, s3, s2
	s_ashr_i32 s3, s2, 31
	s_lshl_b64 s[2:3], s[2:3], 13
	s_add_u32 s2, s20, s2
	s_addc_u32 s3, s21, s3
	v_lshlrev_b32_e32 v154, 1, v169
	v_lshl_add_u64 v[2:3], s[2:3], 0, v[154:155]
	v_add_co_u32_e32 v2, vcc, s23, v2
	s_nop 1
	v_addc_co_u32_e32 v3, vcc, 0, v3, vcc
	v_cvt_pk_f16_f32 v90, v90, v91
	v_cvt_pk_f16_f32 v91, v92, v93
	v_cvt_pk_f16_f32 v92, v94, v95
	v_cvt_pk_f16_f32 v93, v96, v97
	v_cvt_pk_f16_f32 v94, v98, v99
	v_cvt_pk_f16_f32 v95, v100, v101
	v_cvt_pk_f16_f32 v96, v102, v103
	v_cvt_pk_f16_f32 v97, v104, v105
	v_cvt_pk_f16_f32 v106, v106, v107
	v_cvt_pk_f16_f32 v107, v108, v109
	v_cvt_pk_f16_f32 v108, v110, v111
	v_cvt_pk_f16_f32 v109, v112, v113
	v_cvt_pk_f16_f32 v110, v114, v115
	v_cvt_pk_f16_f32 v111, v116, v117
	v_cvt_pk_f16_f32 v112, v118, v119
	v_cvt_pk_f16_f32 v113, v120, v121
	v_xor_b32_e32 v74, 0x18e0, v173
	v_xor_b32_e32 v75, 0x18e0, v172
	ds_write_b128 v74, v[90:93]
	ds_write_b128 v75, v[94:97]
	ds_write_b128 v74, v[106:109] offset:32768
	ds_write_b128 v75, v[110:113] offset:32768
	s_setprio 0
	s_waitcnt lgkmcnt(0)
	s_barrier
	global_load_dwordx4 v[62:65], v154, s[2:3]
	global_load_dwordx4 v[46:49], v154, s[2:3] offset:1024
	global_load_dwordx4 v[42:45], v154, s[2:3] offset:2048
	global_load_dwordx4 v[38:41], v154, s[2:3] offset:3072
	global_load_dwordx4 v[54:57], v[2:3], off offset:1024
	global_load_dwordx4 v[50:53], v[2:3], off offset:2048
	v_lshl_add_u64 v[4:5], s[12:13], 0, v[154:155]
	global_load_dwordx4 v[126:129], v154, s[12:13]
	global_load_dwordx4 v[122:125], v154, s[12:13] offset:1024
	global_load_dwordx4 v[118:121], v154, s[12:13] offset:2048
	global_load_dwordx4 v[114:117], v154, s[12:13] offset:3072
	global_load_dwordx4 v[34:37], v168, s[2:3]
	global_load_dwordx4 v[110:113], v168, s[12:13]
	v_add_co_u32_e32 v4, vcc, s23, v4
	s_nop 1
	v_addc_co_u32_e32 v5, vcc, 0, v5, vcc
	global_load_dwordx4 v[58:61], v[2:3], off offset:3072
	global_load_dwordx4 v[106:109], v[4:5], off offset:1024
	global_load_dwordx4 v[94:97], v[4:5], off offset:2048
	global_load_dwordx4 v[90:93], v[4:5], off offset:3072
	v_bfrev_b32_e32 v3, v156
	v_lshlrev_b32_e32 v7, 5, v167
	v_lshlrev_b32_e32 v6, 9, v167
	v_and_b32_e32 v7, 0x200, v7
	v_lshlrev_b32_e32 v8, 8, v167
	v_lshrrev_b32_e32 v3, 27, v3
	v_lshrrev_b32_e32 v2, 2, v167
	v_lshrrev_b32_e32 v4, 4, v156
	v_xor_b32_e32 v5, v169, v156
	v_and_b32_e32 v6, 0x5800, v6
	v_and_b32_e32 v3, 8, v3
	v_and_or_b32 v7, v8, s24, v7
	v_lshrrev_b32_e32 v5, 1, v5
	v_xor_b32_e32 v4, v2, v4
	v_or3_b32 v3, v7, v6, v3
	v_bitop3_b32 v7, v2, v182, 1 bitop3:0x6c
	v_lshlrev_b32_e32 v2, 1, v167
	v_and_b32_e32 v5, 4, v5
	v_lshlrev_b32_e32 v4, 3, v4
	v_lshrrev_b32_e32 v6, 1, v167
	v_and_b32_e32 v2, 2, v2
	v_and_or_b32 v9, v169, 8, v2
	v_and_b32_e32 v2, 8, v4
	v_and_or_b32 v4, v6, 2, v5
	v_or3_b32 v2, v4, v2, v134
	v_lshlrev_b32_e32 v2, 4, v2
	v_bitop3_b32 v146, v3, s28, v2 bitop3:0x36
	v_xor_b32_e32 v8, v6, v182
	v_xor_b32_e32 v147, 0x2010, v146
	v_lshlrev_b32_e32 v8, 2, v8
	v_and_b32_e32 v8, 4, v8
	v_or3_b32 v6, v9, v7, v8
	v_lshlrev_b32_e32 v7, 11, v167
	v_and_b32_e32 v8, 0x7800, v7
	v_lshlrev_b32_e32 v6, 4, v6
	v_or3_b32 v22, v6, v8, v170
	v_and_b32_e32 v23, 0x8000, v7
	v_xor_b32_e32 v150, 16, v146
	v_xad_u32 v70, v22, s28, v23
	v_xor_b32_e32 v151, 0x2000, v146
	ds_read_b64_tr_b16 v[18:19], v146
	ds_read_b64_tr_b16 v[20:21], v147
	ds_read_b64_tr_b16 v[22:23], v146 offset:32768
	ds_read_b64_tr_b16 v[24:25], v147 offset:32768
	ds_read_b64_tr_b16 v[26:27], v150
	ds_read_b64_tr_b16 v[28:29], v151
	ds_read_b64_tr_b16 v[30:31], v150 offset:32768
	ds_read_b64_tr_b16 v[32:33], v151 offset:32768
	v_xor_b32_e32 v148, 32, v146
	v_xor_b32_e32 v149, 0x2030, v146
	v_xor_b32_e32 v144, 48, v146
	v_xor_b32_e32 v145, 0x2020, v146
	v_xor_b32_e32 v142, 64, v146
	v_xor_b32_e32 v143, 0x2050, v146
	v_xor_b32_e32 v140, 0x50, v146
	v_xor_b32_e32 v141, 0x2040, v146
	v_xor_b32_e32 v138, 0x60, v146
	v_xor_b32_e32 v139, 0x2070, v146
	v_xor_b32_e32 v136, 0x70, v146
	v_xor_b32_e32 v137, 0x2060, v146
	v_xor_b32_e32 v71, 0x60, v70
	s_lshl_b64 s[0:1], s[0:1], 13
	s_add_u32 s0, s8, s0
	s_addc_u32 s1, s9, s1
	s_waitcnt vmcnt(17) lgkmcnt(4)
	v_mfma_f32_32x32x16_f16 v[2:17], v[18:21], v[86:89], 0
	s_waitcnt vmcnt(16)
	v_mfma_f32_32x32x16_f16 v[2:17], v[22:25], v[82:85], v[2:17]
	ds_read_b64_tr_b16 v[206:207], v148
	ds_read_b64_tr_b16 v[208:209], v149
	ds_read_b64_tr_b16 v[210:211], v148 offset:32768
	ds_read_b64_tr_b16 v[212:213], v149 offset:32768
	s_waitcnt lgkmcnt(4)
	v_mfma_f32_32x32x16_f16 v[190:205], v[26:29], v[86:89], 0
	v_mfma_f32_32x32x16_f16 v[190:205], v[30:33], v[82:85], v[190:205]
	s_nop 4
	v_cvt_pk_f16_f32 v2, v2, v3
	v_cvt_pk_f16_f32 v3, v4, v5
	v_cvt_pk_f16_f32 v4, v6, v7
	v_cvt_pk_f16_f32 v5, v8, v9
	v_cvt_pk_f16_f32 v6, v10, v11
	v_cvt_pk_f16_f32 v7, v12, v13
	v_cvt_pk_f16_f32 v8, v14, v15
	v_cvt_pk_f16_f32 v9, v16, v17
	v_xor_b32_e32 v73, 0x280, v70
	ds_write_b128 v70, v[2:5]
	ds_write_b128 v73, v[6:9]
	ds_read_b64_tr_b16 v[18:19], v144
	ds_read_b64_tr_b16 v[20:21], v145
	ds_read_b64_tr_b16 v[22:23], v144 offset:32768
	ds_read_b64_tr_b16 v[24:25], v145 offset:32768
	s_waitcnt lgkmcnt(6)
	v_mfma_f32_32x32x16_f16 v[2:17], v[206:209], v[86:89], 0
	v_mfma_f32_32x32x16_f16 v[2:17], v[210:213], v[82:85], v[2:17]
	v_cvt_pk_f16_f32 v190, v190, v191
	v_cvt_pk_f16_f32 v191, v192, v193
	v_cvt_pk_f16_f32 v192, v194, v195
	v_cvt_pk_f16_f32 v193, v196, v197
	v_cvt_pk_f16_f32 v194, v198, v199
	v_cvt_pk_f16_f32 v195, v200, v201
	v_cvt_pk_f16_f32 v196, v202, v203
	v_cvt_pk_f16_f32 v197, v204, v205
	v_xor_b32_e32 v72, 16, v70
	v_xor_b32_e32 v73, 0x290, v70
	ds_write_b128 v72, v[190:193]
	ds_write_b128 v73, v[194:197]
	ds_read_b64_tr_b16 v[26:27], v142
	ds_read_b64_tr_b16 v[28:29], v143
	ds_read_b64_tr_b16 v[30:31], v142 offset:32768
	ds_read_b64_tr_b16 v[32:33], v143 offset:32768
	s_waitcnt lgkmcnt(6)
	v_mfma_f32_32x32x16_f16 v[190:205], v[18:21], v[86:89], 0
	v_mfma_f32_32x32x16_f16 v[190:205], v[22:25], v[82:85], v[190:205]
	v_cvt_pk_f16_f32 v2, v2, v3
	v_cvt_pk_f16_f32 v3, v4, v5
	v_cvt_pk_f16_f32 v4, v6, v7
	v_cvt_pk_f16_f32 v5, v8, v9
	v_cvt_pk_f16_f32 v6, v10, v11
	v_cvt_pk_f16_f32 v7, v12, v13
	v_cvt_pk_f16_f32 v8, v14, v15
	v_cvt_pk_f16_f32 v9, v16, v17
	v_xor_b32_e32 v72, 32, v70
	v_xor_b32_e32 v73, 0x2a0, v70
	ds_write_b128 v72, v[2:5]
	ds_write_b128 v73, v[6:9]
	ds_read_b64_tr_b16 v[206:207], v140
	ds_read_b64_tr_b16 v[208:209], v141
	ds_read_b64_tr_b16 v[210:211], v140 offset:32768
	ds_read_b64_tr_b16 v[212:213], v141 offset:32768
	s_waitcnt lgkmcnt(6)
	v_mfma_f32_32x32x16_f16 v[2:17], v[26:29], v[86:89], 0
	v_mfma_f32_32x32x16_f16 v[2:17], v[30:33], v[82:85], v[2:17]
	v_cvt_pk_f16_f32 v190, v190, v191
	v_cvt_pk_f16_f32 v191, v192, v193
	v_cvt_pk_f16_f32 v192, v194, v195
	v_cvt_pk_f16_f32 v193, v196, v197
	v_cvt_pk_f16_f32 v194, v198, v199
	v_cvt_pk_f16_f32 v195, v200, v201
	v_cvt_pk_f16_f32 v196, v202, v203
	v_cvt_pk_f16_f32 v197, v204, v205
	v_xor_b32_e32 v72, 48, v70
	v_xor_b32_e32 v73, 0x2b0, v70
	ds_write_b128 v72, v[190:193]
	ds_write_b128 v73, v[194:197]
	ds_read_b64_tr_b16 v[18:19], v138
	ds_read_b64_tr_b16 v[20:21], v139
	ds_read_b64_tr_b16 v[22:23], v138 offset:32768
	ds_read_b64_tr_b16 v[24:25], v139 offset:32768
	s_waitcnt lgkmcnt(6)
	v_mfma_f32_32x32x16_f16 v[190:205], v[206:209], v[86:89], 0
	v_mfma_f32_32x32x16_f16 v[190:205], v[210:213], v[82:85], v[190:205]
	v_cvt_pk_f16_f32 v2, v2, v3
	v_cvt_pk_f16_f32 v3, v4, v5
	v_cvt_pk_f16_f32 v4, v6, v7
	v_cvt_pk_f16_f32 v5, v8, v9
	v_cvt_pk_f16_f32 v6, v10, v11
	v_cvt_pk_f16_f32 v7, v12, v13
	v_cvt_pk_f16_f32 v8, v14, v15
	v_cvt_pk_f16_f32 v9, v16, v17
	v_xor_b32_e32 v72, 64, v70
	v_xor_b32_e32 v73, 0x2c0, v70
	ds_write_b128 v72, v[2:5]
	ds_write_b128 v73, v[6:9]
	ds_read_b64_tr_b16 v[26:27], v136
	ds_read_b64_tr_b16 v[28:29], v137
	ds_read_b64_tr_b16 v[30:31], v136 offset:32768
	ds_read_b64_tr_b16 v[32:33], v137 offset:32768
	s_waitcnt lgkmcnt(6)
	v_mfma_f32_32x32x16_f16 v[2:17], v[18:21], v[86:89], 0
	v_mfma_f32_32x32x16_f16 v[2:17], v[22:25], v[82:85], v[2:17]
	v_cvt_pk_f16_f32 v190, v190, v191
	v_cvt_pk_f16_f32 v191, v192, v193
	v_cvt_pk_f16_f32 v192, v194, v195
	v_cvt_pk_f16_f32 v193, v196, v197
	v_cvt_pk_f16_f32 v194, v198, v199
	v_cvt_pk_f16_f32 v195, v200, v201
	v_cvt_pk_f16_f32 v196, v202, v203
	v_cvt_pk_f16_f32 v197, v204, v205
	v_xor_b32_e32 v72, 0x50, v70
	v_xor_b32_e32 v73, 0x2d0, v70
	ds_write_b128 v72, v[190:193]
	ds_write_b128 v73, v[194:197]
	s_waitcnt lgkmcnt(2)
	v_mfma_f32_32x32x16_f16 v[190:205], v[26:29], v[86:89], 0
	v_mfma_f32_32x32x16_f16 v[190:205], v[30:33], v[82:85], v[190:205]
	v_cvt_pk_f16_f32 v2, v2, v3
	v_cvt_pk_f16_f32 v3, v4, v5
	v_cvt_pk_f16_f32 v4, v6, v7
	v_cvt_pk_f16_f32 v5, v8, v9
	v_cvt_pk_f16_f32 v6, v10, v11
	v_cvt_pk_f16_f32 v7, v12, v13
	v_cvt_pk_f16_f32 v8, v14, v15
	v_cvt_pk_f16_f32 v9, v16, v17
	v_xor_b32_e32 v72, 0x60, v70
	v_xor_b32_e32 v73, 0x2e0, v70
	ds_write_b128 v72, v[2:5]
	ds_write_b128 v73, v[6:9]
	v_cvt_pk_f16_f32 v190, v190, v191
	v_cvt_pk_f16_f32 v191, v192, v193
	v_cvt_pk_f16_f32 v192, v194, v195
	v_cvt_pk_f16_f32 v193, v196, v197
	v_cvt_pk_f16_f32 v194, v198, v199
	v_cvt_pk_f16_f32 v195, v200, v201
	v_cvt_pk_f16_f32 v196, v202, v203
	v_cvt_pk_f16_f32 v197, v204, v205
	v_xor_b32_e32 v72, 0x70, v70
	v_xor_b32_e32 v73, 0x2f0, v70
	ds_write_b128 v72, v[190:193]
	ds_write_b128 v73, v[194:197]
	v_lshl_add_u64 v[2:3], s[0:1], 0, v[154:155]
	v_lshl_add_u64 v[4:5], v[2:3], 0, s[18:19]
	v_add_co_u32_e32 v2, vcc, s25, v2
	s_waitcnt lgkmcnt(0)
	s_nop 0
	v_addc_co_u32_e32 v3, vcc, 0, v3, vcc
	s_barrier
	s_nop 0
	s_nop 0
	global_load_dwordx4 v[102:105], v[2:3], off
	global_load_dwordx4 v[98:101], v[4:5], off offset:1024
	s_setprio 1
	s_add_u32 s0, s2, 0x2000
	s_addc_u32 s1, s3, 0
	v_lshl_add_u64 v[2:3], s[0:1], 0, v[154:155]
	v_add_co_u32_e32 v2, vcc, s23, v2
	global_load_dwordx4 v[66:69], v154, s[0:1]
	global_load_dwordx4 v[70:73], v154, s[0:1] offset:1024
	global_load_dwordx4 v[74:77], v154, s[0:1] offset:2048
	global_load_dwordx4 v[78:81], v154, s[0:1] offset:3072
	v_addc_co_u32_e32 v3, vcc, 0, v3, vcc
	global_load_dwordx4 v[82:85], v168, s[0:1]
	global_load_dwordx4 v[86:89], v[2:3], off offset:1024
	global_load_dwordx4 v[182:185], v[2:3], off offset:2048
	global_load_dwordx4 v[186:189], v[2:3], off offset:3072
	ds_read_b128 v[18:21], v179
	ds_read_b128 v[22:25], v179 offset:32768
	ds_read_b128 v[26:29], v178
	ds_read_b128 v[30:33], v178 offset:32768
	s_add_u32 s0, s2, 0x6000
	s_addc_u32 s1, s3, 0
	s_waitcnt vmcnt(25) lgkmcnt(3)
	v_mfma_f32_32x32x16_f16 v[2:17], v[18:21], v[62:65], 0
	s_add_u32 s2, s2, 0x4000
	s_addc_u32 s3, s3, 0
	s_or_b32 s27, s26, 0x8a0
	s_or_b32 s26, s26, 0xa20
	s_waitcnt vmcnt(24) lgkmcnt(1)
	v_mfma_f32_32x32x16_f16 v[2:17], v[26:29], v[46:49], v[2:17]
	s_waitcnt vmcnt(23)
	v_mfma_f32_32x32x16_f16 v[2:17], v[22:25], v[42:45], v[2:17]
	s_waitcnt vmcnt(22) lgkmcnt(0)
	v_mfma_f32_32x32x16_f16 v[2:17], v[30:33], v[38:41], v[2:17]
	s_waitcnt vmcnt(15)
	v_mfma_f32_32x32x16_f16 v[34:49], v[18:21], v[34:37], 0
	s_nop 9
	v_cvt_pk_f16_f32 v9, v8, v9
	v_cvt_pk_f16_f32 v8, v6, v7
	v_cvt_pk_f16_f32 v7, v4, v5
	v_cvt_pk_f16_f32 v6, v2, v3
	v_cvt_pk_f16_f32 v5, v16, v17
	v_cvt_pk_f16_f32 v4, v14, v15
	v_cvt_pk_f16_f32 v3, v12, v13
	v_mfma_f32_32x32x16_f16 v[34:49], v[26:29], v[54:57], v[34:49]
	v_cvt_pk_f16_f32 v2, v10, v11
	v_mfma_f32_32x32x16_f16 v[34:49], v[22:25], v[50:53], v[34:49]
	s_waitcnt vmcnt(13)
	v_mfma_f32_32x32x16_f16 v[34:49], v[30:33], v[58:61], v[34:49]
	v_mfma_f32_32x32x16_f16 v[18:33], v[6:9], v[126:129], 0
	s_nop 10
	v_cvt_pk_f16_f32 v13, v40, v41
	v_cvt_pk_f16_f32 v12, v38, v39
	v_cvt_pk_f16_f32 v11, v36, v37
	v_cvt_pk_f16_f32 v10, v34, v35
	v_cvt_pk_f16_f32 v17, v48, v49
	v_cvt_pk_f16_f32 v16, v46, v47
	v_cvt_pk_f16_f32 v15, v44, v45
	v_mfma_f32_32x32x16_f16 v[50:65], v[6:9], v[110:113], 0
	v_bitop3_b32 v6, v171, s27, v170 bitop3:0x36
	v_cvt_pk_f16_f32 v14, v42, v43
	v_mfma_f32_32x32x16_f16 v[18:33], v[2:5], v[122:125], v[18:33]
	s_waitcnt vmcnt(12)
	v_mfma_f32_32x32x16_f16 v[50:65], v[2:5], v[106:109], v[50:65]
	ds_read_b128 v[2:5], v6
	ds_read_b128 v[6:9], v6 offset:32768
	v_mfma_f32_32x32x16_f16 v[18:33], v[10:13], v[118:121], v[18:33]
	s_waitcnt vmcnt(11)
	v_mfma_f32_32x32x16_f16 v[50:65], v[10:13], v[94:97], v[50:65]
	s_waitcnt vmcnt(7) lgkmcnt(1)
	v_mfma_f32_32x32x16_f16 v[34:49], v[2:5], v[66:69], 0
	v_mfma_f32_32x32x16_f16 v[18:33], v[14:17], v[114:117], v[18:33]
	v_mfma_f32_32x32x16_f16 v[50:65], v[14:17], v[90:93], v[50:65]
	v_bitop3_b32 v14, v171, s26, v170 bitop3:0x36
	ds_read_b128 v[10:13], v14
	ds_read_b128 v[14:17], v14 offset:32768
	s_nop 7
	v_cvt_pk_f16_f32 v25, v24, v25
	v_cvt_pk_f16_f32 v24, v22, v23
	v_cvt_pk_f16_f32 v23, v20, v21
	v_cvt_pk_f16_f32 v22, v18, v19
	v_cvt_pk_f16_f32 v21, v32, v33
	s_waitcnt vmcnt(6) lgkmcnt(1)
	v_mfma_f32_32x32x16_f16 v[34:49], v[10:13], v[70:73], v[34:49]
	v_cvt_pk_f16_f32 v20, v30, v31
	v_cvt_pk_f16_f32 v19, v28, v29
	v_cvt_pk_f16_f32 v18, v26, v27
	ds_write_b128 v173, v[22:25]
	ds_write_b128 v172, v[18:21]
	v_cvt_pk_f16_f32 v21, v56, v57
	v_cvt_pk_f16_f32 v20, v54, v55
	s_waitcnt vmcnt(5)
	v_mfma_f32_32x32x16_f16 v[34:49], v[6:9], v[74:77], v[34:49]
	v_cvt_pk_f16_f32 v19, v52, v53
	v_cvt_pk_f16_f32 v18, v50, v51
	ds_write_b128 v173, v[18:21] offset:32768
	v_cvt_pk_f16_f32 v21, v64, v65
	v_cvt_pk_f16_f32 v20, v62, v63
	v_cvt_pk_f16_f32 v19, v60, v61
	v_cvt_pk_f16_f32 v18, v58, v59
	s_waitcnt vmcnt(4) lgkmcnt(3)
	v_mfma_f32_32x32x16_f16 v[34:49], v[14:17], v[78:81], v[34:49]
	ds_write_b128 v172, v[18:21] offset:32768
	s_waitcnt vmcnt(3)
	v_mfma_f32_32x32x16_f16 v[66:81], v[2:5], v[82:85], 0
	s_nop 8
	v_cvt_pk_f16_f32 v41, v40, v41
	v_cvt_pk_f16_f32 v40, v38, v39
	v_cvt_pk_f16_f32 v39, v36, v37
	v_cvt_pk_f16_f32 v38, v34, v35
	v_cvt_pk_f16_f32 v85, v48, v49
	v_cvt_pk_f16_f32 v84, v46, v47
	v_cvt_pk_f16_f32 v83, v44, v45
	s_waitcnt vmcnt(2)
	v_mfma_f32_32x32x16_f16 v[66:81], v[10:13], v[86:89], v[66:81]
	v_cvt_pk_f16_f32 v82, v42, v43
	s_waitcnt vmcnt(1)
	v_mfma_f32_32x32x16_f16 v[66:81], v[6:9], v[182:185], v[66:81]
	s_waitcnt vmcnt(0)
	v_mfma_f32_32x32x16_f16 v[66:81], v[14:17], v[186:189], v[66:81]
	v_mfma_f32_32x32x16_f16 v[2:17], v[38:41], v[126:129], 0
	s_nop 10
	v_cvt_pk_f16_f32 v73, v72, v73
	v_cvt_pk_f16_f32 v72, v70, v71
	v_cvt_pk_f16_f32 v70, v66, v67
	v_cvt_pk_f16_f32 v67, v76, v77
	v_cvt_pk_f16_f32 v66, v74, v75
	global_load_dwordx4 v[74:77], v154, s[2:3]
	v_cvt_pk_f16_f32 v71, v68, v69
	v_cvt_pk_f16_f32 v69, v80, v81
	v_cvt_pk_f16_f32 v68, v78, v79
	global_load_dwordx4 v[78:81], v154, s[2:3] offset:1024
	ds_read_b128 v[18:21], v180
	ds_read_b128 v[22:25], v176
	ds_read_b128 v[26:29], v180 offset:32768
	global_load_dwordx4 v[30:33], v154, s[2:3] offset:2048
	v_mfma_f32_32x32x16_f16 v[34:49], v[38:41], v[110:113], 0
	v_mfma_f32_32x32x16_f16 v[2:17], v[82:85], v[122:125], v[2:17]
	v_mfma_f32_32x32x16_f16 v[34:49], v[82:85], v[106:109], v[34:49]
	ds_read_b128 v[82:85], v176 offset:32768
	s_waitcnt vmcnt(2) lgkmcnt(3)
	v_mfma_f32_32x32x16_f16 v[50:65], v[18:21], v[74:77], 0
	v_mfma_f32_32x32x16_f16 v[2:17], v[70:73], v[118:121], v[2:17]
	v_mfma_f32_32x32x16_f16 v[34:49], v[70:73], v[94:97], v[34:49]
	v_lshl_add_u64 v[70:71], s[2:3], 0, v[154:155]
	v_add_co_u32_e32 v152, vcc, s23, v70
	s_nop 1
	v_addc_co_u32_e32 v153, vcc, 0, v71, vcc
	s_waitcnt vmcnt(1) lgkmcnt(2)
	v_mfma_f32_32x32x16_f16 v[50:65], v[22:25], v[78:81], v[50:65]
	v_mfma_f32_32x32x16_f16 v[2:17], v[66:69], v[114:117], v[2:17]
	v_mfma_f32_32x32x16_f16 v[34:49], v[66:69], v[90:93], v[34:49]
	global_load_dwordx4 v[66:69], v154, s[2:3] offset:3072
	s_nop 9
	v_cvt_pk_f16_f32 v9, v8, v9
	v_cvt_pk_f16_f32 v8, v6, v7
	v_cvt_pk_f16_f32 v7, v4, v5
	v_cvt_pk_f16_f32 v6, v2, v3
	v_cvt_pk_f16_f32 v5, v16, v17
	v_cvt_pk_f16_f32 v4, v14, v15
	s_waitcnt vmcnt(1) lgkmcnt(1)
	v_mfma_f32_32x32x16_f16 v[50:65], v[26:29], v[30:33], v[50:65]
	global_load_dwordx4 v[30:33], v168, s[2:3]
	global_load_dwordx4 v[86:89], v[152:153], off offset:1024
	s_nop 0
	global_load_dwordx4 v[168:171], v168, s[0:1]
	v_cvt_pk_f16_f32 v3, v12, v13
	v_cvt_pk_f16_f32 v2, v10, v11
	ds_write_b128 v175, v[6:9]
	ds_write_b128 v174, v[2:5]
	v_cvt_pk_f16_f32 v5, v40, v41
	s_waitcnt vmcnt(3) lgkmcnt(2)
	v_mfma_f32_32x32x16_f16 v[50:65], v[82:85], v[66:69], v[50:65]
	global_load_dwordx4 v[182:185], v154, s[0:1] offset:1024
	v_cvt_pk_f16_f32 v4, v38, v39
	v_cvt_pk_f16_f32 v3, v36, v37
	v_cvt_pk_f16_f32 v2, v34, v35
	ds_write_b128 v175, v[2:5] offset:32768
	v_cvt_pk_f16_f32 v5, v48, v49
	v_cvt_pk_f16_f32 v4, v46, v47
	s_waitcnt vmcnt(3)
	v_mfma_f32_32x32x16_f16 v[66:81], v[18:21], v[30:33], 0
	global_load_dwordx4 v[18:21], v[152:153], off offset:2048
	v_cvt_pk_f16_f32 v3, v44, v45
	v_cvt_pk_f16_f32 v2, v42, v43
	ds_write_b128 v174, v[2:5] offset:32768
	v_cvt_pk_f16_f32 v57, v56, v57
	v_cvt_pk_f16_f32 v56, v54, v55
	v_cvt_pk_f16_f32 v55, v52, v53
	s_waitcnt vmcnt(3)
	v_mfma_f32_32x32x16_f16 v[66:81], v[22:25], v[86:89], v[66:81]
	global_load_dwordx4 v[22:25], v[152:153], off offset:3072
	v_cvt_pk_f16_f32 v54, v50, v51
	s_waitcnt vmcnt(1)
	v_mfma_f32_32x32x16_f16 v[66:81], v[26:29], v[18:21], v[66:81]
	v_lshl_add_u64 v[18:19], s[0:1], 0, v[154:155]
	v_add_co_u32_e32 v152, vcc, s23, v18
	s_nop 1
	v_addc_co_u32_e32 v153, vcc, 0, v19, vcc
	global_load_dwordx4 v[86:89], v[152:153], off offset:1024
	s_waitcnt vmcnt(1)
	v_mfma_f32_32x32x16_f16 v[66:81], v[82:85], v[22:25], v[66:81]
	v_cvt_pk_f16_f32 v85, v64, v65
	v_cvt_pk_f16_f32 v84, v62, v63
	v_cvt_pk_f16_f32 v83, v60, v61
	v_cvt_pk_f16_f32 v82, v58, v59
	v_mfma_f32_32x32x16_f16 v[18:33], v[54:57], v[126:129], 0
	s_nop 6
	v_cvt_pk_f16_f32 v73, v72, v73
	v_cvt_pk_f16_f32 v72, v70, v71
	v_cvt_pk_f16_f32 v70, v66, v67
	v_cvt_pk_f16_f32 v67, v76, v77
	v_cvt_pk_f16_f32 v66, v74, v75
	global_load_dwordx4 v[74:77], v154, s[0:1]
	ds_read_b128 v[2:5], v181
	ds_read_b128 v[6:9], v177
	ds_read_b128 v[10:13], v181 offset:32768
	global_load_dwordx4 v[14:17], v154, s[0:1] offset:2048
	global_load_dwordx4 v[34:37], v154, s[0:1] offset:3072
	v_mfma_f32_32x32x16_f16 v[50:65], v[54:57], v[110:113], 0
	v_cvt_pk_f16_f32 v71, v68, v69
	v_cvt_pk_f16_f32 v69, v80, v81
	v_cvt_pk_f16_f32 v68, v78, v79
	v_mfma_f32_32x32x16_f16 v[18:33], v[82:85], v[122:125], v[18:33]
	v_mfma_f32_32x32x16_f16 v[50:65], v[82:85], v[106:109], v[50:65]
	ds_read_b128 v[82:85], v177 offset:32768
	v_mfma_f32_32x32x16_f16 v[18:33], v[70:73], v[118:121], v[18:33]
	v_mfma_f32_32x32x16_f16 v[50:65], v[70:73], v[94:97], v[50:65]
	v_mfma_f32_32x32x16_f16 v[18:33], v[66:69], v[114:117], v[18:33]
	v_mfma_f32_32x32x16_f16 v[50:65], v[66:69], v[90:93], v[50:65]
	s_nop 10
	v_cvt_pk_f16_f32 v25, v24, v25
	v_cvt_pk_f16_f32 v24, v22, v23
	v_cvt_pk_f16_f32 v23, v20, v21
	v_cvt_pk_f16_f32 v22, v18, v19
	ds_write_b128 v132, v[22:25]
	s_waitcnt vmcnt(2) lgkmcnt(4)
	v_mfma_f32_32x32x16_f16 v[66:81], v[2:5], v[74:77], 0
	s_waitcnt lgkmcnt(3)
	v_mfma_f32_32x32x16_f16 v[66:81], v[6:9], v[182:185], v[66:81]
	s_waitcnt vmcnt(1) lgkmcnt(2)
	v_mfma_f32_32x32x16_f16 v[66:81], v[10:13], v[14:17], v[66:81]
	s_waitcnt vmcnt(0) lgkmcnt(1)
	v_mfma_f32_32x32x16_f16 v[66:81], v[82:85], v[34:37], v[66:81]
	v_mfma_f32_32x32x16_f16 v[34:49], v[2:5], v[168:171], 0
	global_load_dwordx4 v[2:5], v[152:153], off offset:2048
	s_nop 9
	v_cvt_pk_f16_f32 v73, v72, v73
	v_cvt_pk_f16_f32 v72, v70, v71
	v_cvt_pk_f16_f32 v71, v68, v69
	v_cvt_pk_f16_f32 v70, v66, v67
	v_cvt_pk_f16_f32 v69, v80, v81
	v_cvt_pk_f16_f32 v68, v78, v79
	v_mfma_f32_32x32x16_f16 v[34:49], v[6:9], v[86:89], v[34:49]
	global_load_dwordx4 v[6:9], v[152:153], off offset:3072
	v_cvt_pk_f16_f32 v67, v76, v77
	v_cvt_pk_f16_f32 v66, v74, v75
	s_waitcnt vmcnt(1)
	v_mfma_f32_32x32x16_f16 v[34:49], v[10:13], v[2:5], v[34:49]
	s_waitcnt vmcnt(0)
	v_mfma_f32_32x32x16_f16 v[34:49], v[82:85], v[6:9], v[34:49]
	v_mfma_f32_32x32x16_f16 v[2:17], v[70:73], v[126:129], 0
	s_nop 10
	v_cvt_pk_f16_f32 v41, v40, v41
	v_cvt_pk_f16_f32 v40, v38, v39
	v_cvt_pk_f16_f32 v38, v34, v35
	v_cvt_pk_f16_f32 v35, v44, v45
	v_cvt_pk_f16_f32 v34, v42, v43
	v_cvt_pk_f16_f32 v45, v32, v33
	v_cvt_pk_f16_f32 v44, v30, v31
	v_cvt_pk_f16_f32 v43, v28, v29
	v_cvt_pk_f16_f32 v42, v26, v27
	v_mfma_f32_32x32x16_f16 v[18:33], v[70:73], v[110:113], 0
	v_cvt_pk_f16_f32 v39, v36, v37
	v_cvt_pk_f16_f32 v37, v48, v49
	v_cvt_pk_f16_f32 v36, v46, v47
	ds_write_b128 v131, v[42:45]
	v_cvt_pk_f16_f32 v45, v56, v57
	v_cvt_pk_f16_f32 v44, v54, v55
	v_cvt_pk_f16_f32 v43, v52, v53
	v_mfma_f32_32x32x16_f16 v[2:17], v[66:69], v[122:125], v[2:17]
	v_cvt_pk_f16_f32 v42, v50, v51
	ds_write_b128 v132, v[42:45] offset:32768
	v_cvt_pk_f16_f32 v45, v64, v65
	v_cvt_pk_f16_f32 v44, v62, v63
	v_cvt_pk_f16_f32 v43, v60, v61
	v_cvt_pk_f16_f32 v42, v58, v59
	ds_write_b128 v131, v[42:45] offset:32768
	v_mfma_f32_32x32x16_f16 v[18:33], v[66:69], v[106:109], v[18:33]
	v_mfma_f32_32x32x16_f16 v[2:17], v[38:41], v[118:121], v[2:17]
	v_mfma_f32_32x32x16_f16 v[18:33], v[38:41], v[94:97], v[18:33]
	v_mfma_f32_32x32x16_f16 v[2:17], v[34:37], v[114:117], v[2:17]
	v_mfma_f32_32x32x16_f16 v[18:33], v[34:37], v[90:93], v[18:33]
	s_nop 10
	v_cvt_pk_f16_f32 v9, v8, v9
	v_cvt_pk_f16_f32 v8, v6, v7
	v_cvt_pk_f16_f32 v7, v4, v5
	v_cvt_pk_f16_f32 v6, v2, v3
	v_cvt_pk_f16_f32 v5, v16, v17
	v_cvt_pk_f16_f32 v4, v14, v15
	v_cvt_pk_f16_f32 v3, v12, v13
	v_cvt_pk_f16_f32 v2, v10, v11
	ds_write_b128 v135, v[6:9]
	ds_write_b128 v133, v[2:5]
	v_cvt_pk_f16_f32 v5, v24, v25
	v_cvt_pk_f16_f32 v4, v22, v23
	v_cvt_pk_f16_f32 v3, v20, v21
	v_cvt_pk_f16_f32 v2, v18, v19
	ds_write_b128 v135, v[2:5] offset:32768
	v_cvt_pk_f16_f32 v5, v32, v33
	v_cvt_pk_f16_f32 v4, v30, v31
	v_cvt_pk_f16_f32 v3, v28, v29
	v_cvt_pk_f16_f32 v2, v26, v27
	ds_write_b128 v133, v[2:5] offset:32768
	s_setprio 0
	s_waitcnt lgkmcnt(0)
	s_barrier
	s_cmp_lt_i32 s22, 0
	s_cbranch_scc0 .Lno_pref
	s_add_u32 s36, s10, 0x140000
	s_addc_u32 s37, s11, 0
	v_lshlrev_b32_e32 v192, 3, v156
	v_lshlrev_b32_e32 v193, 3, v167
	global_load_dwordx2 v[190:191], v192, s[36:37]
	global_load_dwordx2 v[194:195], v193, s[36:37] offset:2048
.Lno_pref:
	ds_read_b64_tr_b16 v[2:3], v146
	ds_read_b64_tr_b16 v[4:5], v147
	ds_read_b64_tr_b16 v[36:37], v147 offset:32768
	ds_read_b64_tr_b16 v[34:35], v146 offset:32768
	ds_read_b64_tr_b16 v[18:19], v150
	ds_read_b64_tr_b16 v[20:21], v151
	ds_read_b64_tr_b16 v[40:41], v151 offset:32768
	ds_read_b64_tr_b16 v[38:39], v150 offset:32768
	s_waitcnt lgkmcnt(6)
	v_mfma_f32_32x32x16_f16 v[2:17], v[2:5], v[102:105], 0
	ds_read_b64_tr_b16 v[42:43], v148
	ds_read_b64_tr_b16 v[44:45], v149
	ds_read_b64_tr_b16 v[48:49], v149 offset:32768
	ds_read_b64_tr_b16 v[46:47], v148 offset:32768
	v_cmp_gt_u32_e64 s[0:1], 32, v167
	s_cmp_eq_u32 s5, 0
	v_cmp_lt_i32_e64 s[2:3], v162, v163
	s_waitcnt lgkmcnt(6)
	v_mfma_f32_32x32x16_f16 v[18:33], v[18:21], v[102:105], 0
	v_mfma_f32_32x32x16_f16 v[2:17], v[34:37], v[98:101], v[2:17]
	s_waitcnt lgkmcnt(4)
	v_mfma_f32_32x32x16_f16 v[18:33], v[38:41], v[98:101], v[18:33]
	s_nop 9
	v_mul_f32_e64 v34, v16, v16
	v_mul_f32_e64 v35, v17, v17
	v_mul_f32_e64 v36, v12, v12
	v_mul_f32_e64 v37, v13, v13
	v_mul_f32_e64 v50, v8, v8
	v_mul_f32_e64 v51, v9, v9
	v_pk_mul_f32 v[52:53], v[4:5], v[4:5]
	v_pk_fma_f32 v[50:51], v[6:7], v[6:7], v[50:51]
	v_pk_fma_f32 v[52:53], v[2:3], v[2:3], v[52:53]
	v_pk_fma_f32 v[36:37], v[10:11], v[10:11], v[36:37]
	v_pk_fma_f32 v[34:35], v[14:15], v[14:15], v[34:35]
	v_pk_mul_f32 v[116:117], v[24:25], v[24:25]
	v_pk_mul_f32 v[118:119], v[20:21], v[20:21]
	v_pk_add_f32 v[50:51], v[52:53], v[50:51]
	v_pk_add_f32 v[34:35], v[36:37], v[34:35]
	v_pk_mul_f32 v[112:113], v[32:33], v[32:33]
	v_pk_mul_f32 v[114:115], v[28:29], v[28:29]
	v_pk_mul_f32 v[120:121], v[18:19], v[18:19]
	v_pk_fma_f32 v[18:19], v[18:19], v[18:19], v[118:119]
	v_pk_fma_f32 v[20:21], v[22:23], v[22:23], v[116:117]
	v_pk_add_f32 v[34:35], v[50:51], v[34:35]
	v_pk_mul_f32 v[106:107], v[22:23], v[22:23]
	v_pk_add_f32 v[18:19], v[18:19], v[20:21]
	v_pk_fma_f32 v[20:21], v[26:27], v[26:27], v[114:115]
	v_pk_fma_f32 v[22:23], v[30:31], v[30:31], v[112:113]
	v_add_f32_e32 v34, v34, v35
	v_pk_add_f32 v[20:21], v[20:21], v[22:23]
	v_add_f32_e32 v36, 0, v34
	v_pk_mul_f32 v[108:109], v[26:27], v[26:27]
	v_pk_mul_f32 v[110:111], v[30:31], v[30:31]
	v_pk_add_f32 v[34:35], v[18:19], v[20:21]
	s_waitcnt lgkmcnt(2)
	v_mfma_f32_32x32x16_f16 v[18:33], v[42:45], v[102:105], 0
	v_add_f32_e32 v34, v34, v35
	v_add_f32_e32 v54, v36, v34
	v_sub_f32_e32 v55, v36, v34
	ds_read_b64_tr_b16 v[34:35], v144
	ds_read_b64_tr_b16 v[36:37], v145
	ds_read_b64_tr_b16 v[52:53], v145 offset:32768
	ds_read_b64_tr_b16 v[50:51], v144 offset:32768
	v_pk_fma_f32 v[4:5], v[4:5], v[4:5], v[118:119]
	v_pk_fma_f32 v[16:17], v[16:17], v[16:17], v[112:113]
	v_pk_fma_f32 v[14:15], v[14:15], v[14:15], v[110:111]
	s_waitcnt lgkmcnt(4)
	v_mfma_f32_32x32x16_f16 v[18:33], v[46:49], v[98:101], v[18:33]
	v_fma_f32 v12, v12, v12, v114
	v_fma_f32 v13, v13, v13, v115
	v_fma_f32 v10, v10, v10, v108
	v_fma_f32 v11, v11, v11, v109
	v_fma_f32 v8, v8, v8, v116
	v_fma_f32 v9, v9, v9, v117
	v_pk_fma_f32 v[6:7], v[6:7], v[6:7], v[106:107]
	v_pk_fma_f32 v[2:3], v[2:3], v[2:3], v[120:121]
	s_nop 3
	v_pk_mul_f32 v[38:39], v[32:33], v[32:33]
	v_pk_mul_f32 v[40:41], v[28:29], v[28:29]
	v_pk_mul_f32 v[42:43], v[24:25], v[24:25]
	v_pk_mul_f32 v[44:45], v[20:21], v[20:21]
	v_pk_fma_f32 v[42:43], v[22:23], v[22:23], v[42:43]
	v_pk_fma_f32 v[44:45], v[18:19], v[18:19], v[44:45]
	v_pk_fma_f32 v[40:41], v[26:27], v[26:27], v[40:41]
	v_pk_fma_f32 v[38:39], v[30:31], v[30:31], v[38:39]
	v_pk_add_f32 v[42:43], v[44:45], v[42:43]
	v_pk_add_f32 v[38:39], v[40:41], v[38:39]
	v_pk_fma_f32 v[4:5], v[20:21], v[20:21], v[4:5]
	v_pk_add_f32 v[38:39], v[42:43], v[38:39]
	v_pk_fma_f32 v[6:7], v[22:23], v[22:23], v[6:7]
	v_add_f32_e32 v56, v38, v39
	s_waitcnt lgkmcnt(2)
	v_mfma_f32_32x32x16_f16 v[34:49], v[34:37], v[102:105], 0
	v_add_f32_e32 v70, v54, v56
	v_add_f32_e32 v71, v55, v56
	v_sub_f32_e32 v72, v54, v56
	ds_read_b64_tr_b16 v[54:55], v142
	ds_read_b64_tr_b16 v[56:57], v143
	ds_read_b64_tr_b16 v[68:69], v143 offset:32768
	ds_read_b64_tr_b16 v[66:67], v142 offset:32768
	v_pk_fma_f32 v[8:9], v[24:25], v[24:25], v[8:9]
	v_pk_fma_f32 v[10:11], v[26:27], v[26:27], v[10:11]
	v_pk_fma_f32 v[12:13], v[28:29], v[28:29], v[12:13]
	s_waitcnt lgkmcnt(4)
	v_mfma_f32_32x32x16_f16 v[34:49], v[50:53], v[98:101], v[34:49]
	v_fma_f32 v14, v30, v30, v14
	v_fma_f32 v15, v31, v31, v15
	v_fma_f32 v16, v32, v32, v16
	v_fma_f32 v17, v33, v33, v17
	v_fma_f32 v2, v18, v18, v2
	v_fma_f32 v3, v19, v19, v3
	s_nop 5
	v_pk_mul_f32 v[50:51], v[48:49], v[48:49]
	v_pk_mul_f32 v[52:53], v[44:45], v[44:45]
	v_pk_mul_f32 v[58:59], v[40:41], v[40:41]
	v_pk_mul_f32 v[60:61], v[36:37], v[36:37]
	v_pk_fma_f32 v[58:59], v[38:39], v[38:39], v[58:59]
	v_pk_fma_f32 v[60:61], v[34:35], v[34:35], v[60:61]
	v_pk_fma_f32 v[52:53], v[42:43], v[42:43], v[52:53]
	v_pk_fma_f32 v[50:51], v[46:47], v[46:47], v[50:51]
	v_pk_add_f32 v[58:59], v[60:61], v[58:59]
	v_pk_add_f32 v[50:51], v[52:53], v[50:51]
	v_pk_fma_f32 v[4:5], v[36:37], v[36:37], v[4:5]
	v_pk_add_f32 v[50:51], v[58:59], v[50:51]
	v_pk_fma_f32 v[16:17], v[48:49], v[48:49], v[16:17]
	v_add_f32_e32 v73, v50, v51
	s_waitcnt lgkmcnt(2)
	v_mfma_f32_32x32x16_f16 v[50:65], v[54:57], v[102:105], 0
	v_add_f32_e32 v86, v70, v73
	v_sub_f32_e32 v87, v71, v73
	v_sub_f32_e32 v88, v72, v73
	ds_read_b64_tr_b16 v[70:71], v140
	ds_read_b64_tr_b16 v[72:73], v141
	ds_read_b64_tr_b16 v[84:85], v141 offset:32768
	ds_read_b64_tr_b16 v[82:83], v140 offset:32768
	v_pk_fma_f32 v[14:15], v[46:47], v[46:47], v[14:15]
	v_pk_fma_f32 v[12:13], v[44:45], v[44:45], v[12:13]
	v_pk_fma_f32 v[10:11], v[42:43], v[42:43], v[10:11]
	s_waitcnt lgkmcnt(4)
	v_mfma_f32_32x32x16_f16 v[50:65], v[66:69], v[98:101], v[50:65]
	v_fma_f32 v8, v40, v40, v8
	v_fma_f32 v9, v41, v41, v9
	v_fma_f32 v6, v38, v38, v6
	v_fma_f32 v7, v39, v39, v7
	v_fma_f32 v2, v34, v34, v2
	v_fma_f32 v3, v35, v35, v3
	s_nop 5
	v_pk_mul_f32 v[66:67], v[64:65], v[64:65]
	v_pk_mul_f32 v[68:69], v[60:61], v[60:61]
	v_pk_mul_f32 v[74:75], v[56:57], v[56:57]
	v_pk_mul_f32 v[76:77], v[52:53], v[52:53]
	v_pk_fma_f32 v[74:75], v[54:55], v[54:55], v[74:75]
	v_pk_fma_f32 v[76:77], v[50:51], v[50:51], v[76:77]
	v_pk_fma_f32 v[68:69], v[58:59], v[58:59], v[68:69]
	v_pk_fma_f32 v[66:67], v[62:63], v[62:63], v[66:67]
	v_pk_add_f32 v[74:75], v[76:77], v[74:75]
	v_pk_add_f32 v[66:67], v[68:69], v[66:67]
	v_pk_fma_f32 v[4:5], v[52:53], v[52:53], v[4:5]
	v_pk_add_f32 v[66:67], v[74:75], v[66:67]
	v_pk_fma_f32 v[6:7], v[54:55], v[54:55], v[6:7]
	v_add_f32_e32 v89, v66, v67
	s_waitcnt lgkmcnt(2)
	v_mfma_f32_32x32x16_f16 v[66:81], v[70:73], v[102:105], 0
	v_add_f32_e32 v94, v86, v89
	v_add_f32_e32 v126, v87, v89
	v_add_f32_e32 v127, v88, v89
	v_sub_f32_e32 v128, v86, v89
	ds_read_b64_tr_b16 v[86:87], v138
	ds_read_b64_tr_b16 v[88:89], v139
	ds_read_b64_tr_b16 v[124:125], v139 offset:32768
	ds_read_b64_tr_b16 v[122:123], v138 offset:32768
	v_pk_fma_f32 v[8:9], v[56:57], v[56:57], v[8:9]
	v_pk_fma_f32 v[10:11], v[58:59], v[58:59], v[10:11]
	s_waitcnt lgkmcnt(4)
	v_mfma_f32_32x32x16_f16 v[66:81], v[82:85], v[98:101], v[66:81]
	v_fma_f32 v12, v60, v60, v12
	v_fma_f32 v13, v61, v61, v13
	v_fma_f32 v14, v62, v62, v14
	v_fma_f32 v15, v63, v63, v15
	v_fma_f32 v16, v64, v64, v16
	v_fma_f32 v17, v65, v65, v17
	v_pk_fma_f32 v[2:3], v[50:51], v[50:51], v[2:3]
	s_nop 4
	v_pk_mul_f32 v[82:83], v[80:81], v[80:81]
	v_pk_mul_f32 v[84:85], v[76:77], v[76:77]
	v_pk_mul_f32 v[90:91], v[72:73], v[72:73]
	v_pk_mul_f32 v[92:93], v[68:69], v[68:69]
	v_pk_fma_f32 v[90:91], v[70:71], v[70:71], v[90:91]
	v_pk_fma_f32 v[92:93], v[66:67], v[66:67], v[92:93]
	v_pk_fma_f32 v[84:85], v[74:75], v[74:75], v[84:85]
	v_pk_fma_f32 v[82:83], v[78:79], v[78:79], v[82:83]
	v_pk_add_f32 v[90:91], v[92:93], v[90:91]
	v_pk_add_f32 v[82:83], v[84:85], v[82:83]
	v_pk_fma_f32 v[4:5], v[68:69], v[68:69], v[4:5]
	v_pk_add_f32 v[82:83], v[90:91], v[82:83]
	v_pk_fma_f32 v[18:19], v[80:81], v[80:81], v[16:17]
	v_add_f32_e32 v129, v82, v83
	v_add_f32_e32 v131, v94, v129
	s_waitcnt lgkmcnt(2)
	v_mfma_f32_32x32x16_f16 v[82:97], v[86:89], v[102:105], 0
	v_sub_f32_e32 v135, v126, v129
	v_add_f32_e32 v142, v127, v129
	v_sub_f32_e32 v143, v128, v129
	ds_read_b64_tr_b16 v[126:127], v136
	ds_read_b64_tr_b16 v[128:129], v137
	ds_read_b64_tr_b16 v[138:139], v137 offset:32768
	ds_read_b64_tr_b16 v[136:137], v136 offset:32768
	v_pk_fma_f32 v[20:21], v[78:79], v[78:79], v[14:15]
	v_pk_fma_f32 v[22:23], v[76:77], v[76:77], v[12:13]
	v_pk_fma_f32 v[24:25], v[74:75], v[74:75], v[10:11]
	s_waitcnt lgkmcnt(4)
	v_mfma_f32_32x32x16_f16 v[82:97], v[122:125], v[98:101], v[82:97]
	v_fma_f32 v26, v72, v72, v8
	v_fma_f32 v27, v73, v73, v9
	v_fma_f32 v28, v70, v70, v6
	v_fma_f32 v29, v71, v71, v7
	v_fma_f32 v30, v66, v66, v2
	v_fma_f32 v31, v67, v67, v3
	s_nop 5
	v_pk_fma_f32 v[32:33], v[84:85], v[84:85], v[4:5]
	s_waitcnt lgkmcnt(2)
	v_mfma_f32_32x32x16_f16 v[2:17], v[126:129], v[102:105], 0
	v_fma_f32 v28, v86, v86, v28
	v_fma_f32 v29, v87, v87, v29
	v_fma_f32 v24, v90, v90, v24
	v_fma_f32 v25, v91, v91, v25
	v_fma_f32 v22, v92, v92, v22
	v_fma_f32 v23, v93, v93, v23
	v_pk_fma_f32 v[20:21], v[94:95], v[94:95], v[20:21]
	v_pk_fma_f32 v[18:19], v[96:97], v[96:97], v[18:19]
	v_pk_fma_f32 v[30:31], v[82:83], v[82:83], v[30:31]
	v_pk_fma_f32 v[26:27], v[88:89], v[88:89], v[26:27]
	s_waitcnt lgkmcnt(0)
	v_mfma_f32_32x32x16_f16 v[2:17], v[136:139], v[98:101], v[2:17]
	v_mul_f32_e64 v122, v96, v96
	v_mul_f32_e64 v123, v97, v97
	v_mul_f32_e64 v124, v92, v92
	v_mul_f32_e64 v125, v93, v93
	v_mul_f32_e64 v132, v88, v88
	v_mul_f32_e64 v133, v89, v89
	v_pk_mul_f32 v[140:141], v[84:85], v[84:85]
	v_pk_fma_f32 v[132:133], v[86:87], v[86:87], v[132:133]
	v_pk_fma_f32 v[140:141], v[82:83], v[82:83], v[140:141]
	v_pk_fma_f32 v[124:125], v[90:91], v[90:91], v[124:125]
	s_nop 1
	v_pk_mul_f32 v[38:39], v[8:9], v[8:9]
	v_pk_mul_f32 v[40:41], v[4:5], v[4:5]
	v_pk_mul_f32 v[34:35], v[16:17], v[16:17]
	v_pk_mul_f32 v[36:37], v[12:13], v[12:13]
	v_pk_fma_f32 v[16:17], v[16:17], v[16:17], v[18:19]
	v_pk_fma_f32 v[18:19], v[14:15], v[14:15], v[20:21]
	v_pk_fma_f32 v[12:13], v[12:13], v[12:13], v[22:23]
	v_pk_fma_f32 v[20:21], v[10:11], v[10:11], v[24:25]
	v_pk_fma_f32 v[22:23], v[6:7], v[6:7], v[28:29]
	v_pk_fma_f32 v[24:25], v[2:3], v[2:3], v[30:31]
	v_pk_fma_f32 v[2:3], v[2:3], v[2:3], v[40:41]
	v_pk_fma_f32 v[6:7], v[6:7], v[6:7], v[38:39]
	v_pk_fma_f32 v[4:5], v[4:5], v[4:5], v[32:33]
	v_pk_add_f32 v[2:3], v[2:3], v[6:7]
	v_pk_fma_f32 v[6:7], v[10:11], v[10:11], v[36:37]
	v_pk_fma_f32 v[10:11], v[14:15], v[14:15], v[34:35]
	v_pk_fma_f32 v[8:9], v[8:9], v[8:9], v[26:27]
	v_pk_add_f32 v[6:7], v[6:7], v[10:11]
	v_sub_f32_e32 v10, v24, v25
	v_add_f32_e32 v11, v25, v24
	v_add_f32_e32 v10, v4, v10
	v_sub_f32_e32 v14, v11, v4
	v_add_f32_e32 v4, v4, v11
	v_sub_f32_e32 v10, v10, v5
	v_sub_f32_e32 v11, v14, v5
	v_add_f32_e32 v4, v5, v4
	v_add_f32_e32 v5, v22, v10
	v_add_f32_e32 v10, v22, v11
	v_sub_f32_e32 v11, v4, v22
	v_add_f32_e32 v4, v22, v4
	v_sub_f32_e32 v5, v5, v23
	v_add_f32_e32 v10, v23, v10
	v_sub_f32_e32 v11, v11, v23
	v_add_f32_e32 v4, v23, v4
	v_add_f32_e32 v5, v8, v5
	v_sub_f32_e32 v10, v10, v8
	v_sub_f32_e32 v11, v11, v8
	v_add_f32_e32 v4, v8, v4
	v_sub_f32_e32 v5, v5, v9
	v_pk_fma_f32 v[122:123], v[94:95], v[94:95], v[122:123]
	v_sub_f32_e32 v8, v10, v9
	v_sub_f32_e32 v10, v11, v9
	v_add_f32_e32 v4, v9, v4
	v_add_f32_e32 v5, v20, v5
	v_pk_add_f32 v[132:133], v[140:141], v[132:133]
	v_pk_add_f32 v[122:123], v[124:125], v[122:123]
	v_add_f32_e32 v8, v20, v8
	v_add_f32_e32 v9, v20, v10
	v_sub_f32_e32 v4, v4, v20
	v_sub_f32_e32 v5, v5, v21
	v_pk_add_f32 v[122:123], v[132:133], v[122:123]
	v_add_f32_e32 v8, v21, v8
	v_add_f32_e32 v9, v21, v9
	v_sub_f32_e32 v4, v4, v21
	v_add_f32_e32 v5, v12, v5
	v_add_f32_e32 v122, v122, v123
	v_pk_add_f32 v[2:3], v[2:3], v[6:7]
	v_sub_f32_e32 v8, v8, v12
	v_add_f32_e32 v9, v12, v9
	v_sub_f32_e32 v4, v4, v12
	v_sub_f32_e32 v5, v5, v13
	v_add_f32_e32 v123, v131, v122
	v_add_f32_e32 v2, v2, v3
	v_sub_f32_e32 v8, v8, v13
	v_add_f32_e32 v9, v13, v9
	v_sub_f32_e32 v4, v4, v13
	v_add_f32_e32 v5, v18, v5
	v_add_f32_e32 v3, v123, v2
	v_add_f32_e32 v8, v18, v8
	v_sub_f32_e32 v9, v9, v18
	v_sub_f32_e32 v4, v4, v18
	v_sub_f32_e32 v5, v5, v19
	v_and_b32_e32 v10, 8, v156
	v_add_f32_e32 v8, v19, v8
	v_sub_f32_e32 v9, v9, v19
	v_sub_f32_e32 v4, v4, v19
	v_add_f32_e32 v5, v16, v5
	v_cmp_eq_u32_e32 vcc, 0, v10
	v_cndmask_b32_e64 v10, -v3, v3, s[0:1]
	s_cselect_b64 s[0:1], -1, 0
	s_bitcmp0_b32 s4, 7
	v_sub_f32_e32 v8, v8, v16
	v_sub_f32_e32 v9, v9, v16
	v_sub_f32_e32 v4, v4, v16
	v_sub_f32_e32 v5, v5, v17
	v_cndmask_b32_e64 v11, -v3, v3, s[0:1]
	s_cselect_b64 s[0:1], -1, 0
	v_and_b32_e32 v16, 32, v156
	v_sub_f32_e32 v8, v8, v17
	v_cndmask_b32_e64 v5, -v5, v5, vcc
	v_cndmask_b32_e64 v12, -v3, v3, s[0:1]
	v_cndmask_b32_e64 v18, v161, v162, s[2:3]
	v_cmp_eq_u32_e64 s[2:3], 0, v16
	v_lshlrev_b32_e32 v18, 2, v18
	v_cmp_eq_u32_e64 s[0:1], 0, v134
	v_cndmask_b32_e64 v16, v11, v5, s[2:3]
	v_cndmask_b32_e64 v5, v5, v11, s[2:3]
	v_cndmask_b32_e64 v11, v8, v12, s[2:3]
	ds_bpermute_b32 v11, v18, v11
	v_and_b32_e32 v14, 2, v156
	v_cndmask_b32_e64 v13, -v3, v3, s[0:1]
	v_cmp_eq_u32_e64 s[0:1], 0, v14
	v_cndmask_b32_e64 v8, v12, v8, s[2:3]
	v_add_f32_e32 v124, v135, v122
	v_cndmask_b32_e64 v14, -v3, v3, s[0:1]
	v_cmp_eq_u32_e64 s[0:1], 0, v130
	v_sub_f32_e32 v4, v4, v17
	s_waitcnt lgkmcnt(0)
	v_add_f32_e32 v8, v8, v11
	v_cndmask_b32_e64 v15, -v3, v3, s[0:1]
	v_cndmask_b32_e64 v11, v14, v10, s[2:3]
	v_cndmask_b32_e64 v10, v10, v14, s[2:3]
	v_sub_f32_e32 v6, v124, v2
	v_sub_f32_e32 v9, v9, v17
	v_cndmask_b32_e64 v3, -v3, v3, vcc
	ds_bpermute_b32 v10, v18, v10
	v_cndmask_b32_e64 v12, v4, v15, s[2:3]
	v_sub_f32_e32 v125, v142, v122
	v_cndmask_b32_e64 v19, v9, v13, s[2:3]
	v_cndmask_b32_e64 v9, v13, v9, s[2:3]
	ds_bpermute_b32 v12, v18, v12
	v_cndmask_b32_e64 v13, v6, v3, s[2:3]
	v_sub_f32_e32 v7, v125, v2
	v_bfe_i32 v17, v156, 5, 1
	ds_bpermute_b32 v5, v18, v5
	ds_bpermute_b32 v13, v18, v13
	v_sub_f32_e32 v122, v143, v122
	v_cndmask_b32_e64 v3, v3, v6, s[2:3]
	v_and_b32_e32 v6, v17, v7
	v_sub_f32_e32 v2, v122, v2
	ds_bpermute_b32 v19, v18, v19
	ds_bpermute_b32 v6, v18, v6
	s_waitcnt lgkmcnt(5)
	v_add_f32_e32 v10, v11, v10
	v_cndmask_b32_e64 v4, v15, v4, s[2:3]
	v_and_b32_e32 v11, v17, v2
	s_waitcnt lgkmcnt(4)
	v_add_f32_e32 v4, v4, v12
	ds_bpermute_b32 v11, v18, v11
	v_and_b32_e32 v12, 16, v156
	v_cmp_lt_i32_e64 s[4:5], v164, v163
	s_waitcnt lgkmcnt(4)
	v_add_f32_e32 v5, v16, v5
	s_waitcnt lgkmcnt(3)
	v_add_f32_e32 v3, v3, v13
	v_cndmask_b32_e64 v13, v161, v164, s[4:5]
	v_cmp_eq_u32_e64 s[4:5], 0, v12
	s_waitcnt lgkmcnt(2)
	v_add_f32_e32 v9, v9, v19
	v_lshlrev_b32_e32 v13, 2, v13
	v_cndmask_b32_e64 v12, v4, v5, s[4:5]
	v_cndmask_b32_e64 v4, v5, v4, s[4:5]
	v_cndmask_b32_e64 v5, 0, v7, s[2:3]
	s_waitcnt lgkmcnt(1)
	v_add_f32_e32 v5, v5, v6
	v_cndmask_b32_e64 v2, 0, v2, s[2:3]
	v_cndmask_b32_e64 v7, v9, v5, s[4:5]
	ds_bpermute_b32 v4, v13, v4
	s_waitcnt lgkmcnt(1)
	v_add_f32_e32 v2, v2, v11
	v_cndmask_b32_e64 v6, v3, v8, s[4:5]
	v_cndmask_b32_e64 v3, v8, v3, s[4:5]
	ds_bpermute_b32 v7, v13, v7
	ds_bpermute_b32 v3, v13, v3
	v_cndmask_b32_e64 v8, v10, v2, s[4:5]
	ds_bpermute_b32 v8, v13, v8
	v_cndmask_b32_e64 v5, v5, v9, s[4:5]
	s_waitcnt lgkmcnt(3)
	v_add_f32_e32 v4, v12, v4
	s_waitcnt lgkmcnt(2)
	v_add_f32_e32 v5, v5, v7
	s_waitcnt lgkmcnt(1)
	v_add_f32_e32 v3, v6, v3
	v_cndmask_b32_e64 v2, v2, v10, s[4:5]
	v_cndmask_b32_e32 v6, v5, v4, vcc
	v_cndmask_b32_e32 v4, v4, v5, vcc
	v_mov_b32_e32 v5, v155
	s_waitcnt lgkmcnt(0)
	v_add_f32_e32 v2, v2, v8
	v_mov_b32_dpp v5, v4 row_mirror row_mask:0xf bank_mask:0xf
	s_nop 1
	v_add_f32_dpp v4, v5, v6 row_half_mirror row_mask:0xf bank_mask:0xf bound_ctrl:1
	v_cndmask_b32_e32 v5, v2, v3, vcc
	v_cndmask_b32_e32 v2, v3, v2, vcc
	v_mov_b32_e32 v3, v155
	s_nop 1
	v_mov_b32_dpp v3, v2 row_mirror row_mask:0xf bank_mask:0xf
	s_nop 1
	v_add_f32_dpp v2, v3, v5 row_half_mirror row_mask:0xf bank_mask:0xf bound_ctrl:1
	v_cndmask_b32_e64 v3, v2, v4, s[0:1]
	v_cndmask_b32_e64 v2, v4, v2, s[0:1]
	v_mov_b32_e32 v4, v155
	s_nop 1
	v_mov_b32_dpp v4, v2 row_half_mirror row_mask:0xf bank_mask:0xf
	s_nop 1
	v_add_f32_dpp v2, v4, v3 quad_perm:[3,2,1,0] row_mask:0xf bank_mask:0xf bound_ctrl:1
	v_and_b32_e32 v4, 3, v156
	v_cmp_eq_u32_e32 vcc, 0, v4
	v_and_b32_e32 v4, 56, v156
	v_add_f32_dpp v2, v2, v2 quad_perm:[2,3,0,1] row_mask:0xf bank_mask:0xf bound_ctrl:1
	v_mov_b32_e32 v3, 0
	v_cmp_ne_u32_e64 s[0:1], 56, v4
	s_and_b64 s[2:3], vcc, s[0:1]
	v_mov_b32_dpp v3, v2 quad_perm:[1,0,3,2] row_mask:0xf bank_mask:0xf
	s_and_saveexec_b64 s[0:1], s[2:3]
	v_and_b32_e32 v4, 0xfc, v156
	v_add_f32_e32 v2, v2, v3
	v_or_b32_e32 v4, v165, v4
	ds_write_b32 v4, v2
	s_or_b64 exec, exec, s[0:1]
	v_cmp_gt_i32_e32 vcc, 14, v156
	s_cmp_lt_i32 s22, 0
	s_cbranch_scc0 .Lno_stage
	v_readfirstlane_b32 s38, v156
	s_waitcnt vmcnt(0)
	v_add_u32_e32 v192, 0x10000, v192
	ds_write_b64 v192, v[190:191]
	s_cmp_lg_u32 s38, 0
	s_cbranch_scc1 .Lno_stage
	ds_write_b64 v192, v[194:195] offset:2048
.Lno_stage:
	s_waitcnt lgkmcnt(0)
	s_barrier
	s_and_saveexec_b64 s[0:1], vcc
	s_cbranch_execz .LBB1_2
	ds_read_b32 v2, v166
	ds_read_b32 v3, v166 offset:64
	ds_read_b32 v4, v166 offset:128
	ds_read_b32 v5, v166 offset:192
	s_waitcnt lgkmcnt(2)
	v_add_f32_e32 v2, v2, v3
	s_waitcnt lgkmcnt(1)
	v_add_f32_e32 v2, v2, v4
	s_waitcnt lgkmcnt(0)
	v_add_f32_e32 v2, v2, v5
	v_mul_f32_e32 v4, 0x39800000, v2
	v_lshl_add_u64 v[2:3], v[156:157], 2, s[14:15]
	global_store_dword v[2:3], v4, off
	s_branch .LBB1_2
